# write-through output stores also in P0 and P4
# baseline (speedup 1.0000x reference)
; #define LAS __attribute__((address_space(3)))
; __device__ __forceinline__ unsigned pk2(float lo, float hi) { return f2bf(lo) | (f2bf(hi) << 16); }
; __device__ __forceinline__ void p0_prologue(const Params& P, LAS unsigned char* lds, int tid, int lane, int wave, int vcu, int G) {
;     ...
;         for (int m = gw; m < T; m += NGW) {
;             const f32x4* xr = (const f32x4*)(P.x + (size_t)m * D) + lane;
;             f32x4 v[4]; float s = 0.f;
; #pragma unroll
;             for (int j = 0; j < 4; ++j) { v[j] = xr[64 * j]; s += (v[j].x * v[j].x + v[j].y * v[j].y) + (v[j].z * v[j].z + v[j].w * v[j].w); }
;             const float rstd = rsqrtf(wave_sum(s) * (1.0f / D) + 1e-6f);
;             v2u* o8 = (v2u*)(XB0 + (size_t)m * D) + lane;
;             float part[8];
; #pragma unroll
;             for (int c = 0; c < 8; ++c) part[c] = 0.f;
; #pragma unroll
;             for (int j = 0; j < 4; ++j) {
;                 v[j] = v[j] * rstd * w4[j];
;                 v2u o; o.x = pk2(v[j].x, v[j].y); o.y = pk2(v[j].z, v[j].w); o8[64 * j] = o;
; #pragma unroll
;                 for (int e = 0; e < 4; ++e) {
;                     const f32x4 wa = *(const LAS f32x4*)(wabl + ((((j * 4 + e) * 2 + 0) * 64 + lane) << 2));
;                     const f32x4 wb = *(const LAS f32x4*)(wabl + ((((j * 4 + e) * 2 + 1) * 64 + lane) << 2));
;                     const float hv = v[j][e];
;                     part[0] += hv * wa.x; part[1] += hv * wa.y; part[2] += hv * wa.z; part[3] += hv * wa.w;
;                     part[4] += hv * wb.x; part[5] += hv * wb.y; part[6] += hv * wb.z; part[7] += hv * wb.w;
;                 }
;             }
; #pragma unroll
;             for (int c = 0; c < 8; ++c) part[c] = wave_sum(part[c]);
;             float o = part[0];
; #pragma unroll
;             for (int c = 1; c < 8; ++c) o = (lane == c) ? part[c] : o;
;             if (lane < 8) AB[(size_t)m * 8 + lane] = o;
.LBB0_18:
	global_load_dwordx4 v[30:33], v[40:41], off offset:-3072
	global_load_dwordx4 v[46:49], v[40:41], off offset:-2048
	global_load_dwordx4 v[22:25], v[40:41], off offset:-1024
	global_load_dwordx4 v[18:21], v[40:41], off
	s_mov_b32 s0, 0x800000
	ds_read_b128 v[50:53], v35
	ds_read_b128 v[62:65], v35 offset:1024
	ds_read_b128 v[26:29], v35 offset:2048
	v_lshl_add_u64 v[42:43], s[24:25], 0, v[38:39]
	s_mov_b32 s18, 0x1c00000
	v_add_co_u32_e64 v42, s[18:19], s18, v42
	s_waitcnt vmcnt(3)
	v_mul_f32_e32 v44, v31, v31
	v_mul_f32_e32 v54, v33, v33
	s_waitcnt vmcnt(2)
	v_mul_f32_e32 v55, v47, v47
	v_mul_f32_e32 v56, v49, v49
	s_waitcnt vmcnt(1)
	v_mul_f32_e32 v57, v23, v23
	v_mul_f32_e32 v58, v25, v25
	v_fmac_f32_e32 v44, v30, v30
	v_fmac_f32_e32 v54, v32, v32
	v_fmac_f32_e32 v55, v46, v46
	v_fmac_f32_e32 v56, v48, v48
	s_waitcnt vmcnt(0)
	v_mul_f32_e32 v59, v19, v19
	v_add_f32_e32 v44, v44, v54
	v_mul_f32_e32 v54, v21, v21
	v_fmac_f32_e32 v57, v22, v22
	v_fmac_f32_e32 v58, v24, v24
	v_add_f32_e32 v55, v55, v56
	v_fmac_f32_e32 v59, v18, v18
	v_fmac_f32_e32 v54, v20, v20
	v_add_f32_e32 v56, v57, v58
	v_add_f32_e32 v44, v44, v55
	v_add_f32_e32 v54, v59, v54
	v_add_f32_e32 v44, v44, v56
	v_add_f32_e32 v44, v44, v54
	v_addc_co_u32_e64 v43, s[18:19], 0, v43, s[18:19]
	s_nop 0
	v_add_f32_dpp v44, v44, v44 quad_perm:[1,0,3,2] row_mask:0xf bank_mask:0xf bound_ctrl:1
	s_nop 1
	v_add_f32_dpp v44, v44, v44 quad_perm:[2,3,0,1] row_mask:0xf bank_mask:0xf bound_ctrl:1
	s_nop 1
	v_add_f32_dpp v44, v44, v44 row_half_mirror row_mask:0xf bank_mask:0xf bound_ctrl:1
	s_nop 1
	v_add_f32_dpp v44, v44, v44 row_mirror row_mask:0xf bank_mask:0xf bound_ctrl:1
	v_mov_b32_e32 v54, v44
	s_nop 1
	v_permlane16_swap_b32_e32 v44, v54
	v_add_f32 v44, v44, v54
	s_nop 1
	s_nop 0
	v_mov_b32_e32 v54, v44
	s_nop 1
	v_permlane32_swap_b32_e32 v44, v54
	v_add_f32 v44, v44, v54
	s_nop 0
	v_fmamk_f32 v44, v44, 0x3a800000, v1
	v_mul_f32_e32 v54, 0x4b800000, v44
	v_cmp_gt_f32_e64 s[0:1], s0, v44
	s_nop 1
	v_cndmask_b32_e64 v44, v44, v54, s[0:1]
	v_rsq_f32_e32 v44, v44
	s_nop 0
	v_mul_f32_e32 v54, 0x45800000, v44
	v_cndmask_b32_e64 v44, v44, v54, s[0:1]
	v_pk_mul_f32 v[30:31], v[30:31], v[44:45] op_sel_hi:[1,0]
	v_pk_mul_f32 v[32:33], v[32:33], v[44:45] op_sel_hi:[1,0]
	v_pk_mul_f32 v[30:31], v[2:3], v[30:31]
	v_pk_mul_f32 v[46:47], v[46:47], v[44:45] op_sel_hi:[1,0]
	s_waitcnt lgkmcnt(2)
	v_fma_f32 v61, v50, v30, 0
	v_fma_f32 v60, v51, v30, 0
	v_fma_f32 v59, v52, v30, 0
	v_fma_f32 v58, v53, v30, 0
	ds_read_b128 v[50:53], v35 offset:3072
	s_waitcnt lgkmcnt(1)
	v_fmac_f32_e32 v61, v26, v31
	v_fmac_f32_e32 v60, v27, v31
	v_fmac_f32_e32 v59, v28, v31
	v_fmac_f32_e32 v58, v29, v31
	ds_read_b128 v[26:29], v35 offset:4096
	v_fma_f32 v57, v62, v30, 0
	v_fma_f32 v56, v63, v30, 0
	v_fma_f32 v55, v64, v30, 0
	v_fma_f32 v54, v65, v30, 0
	s_waitcnt lgkmcnt(1)
	v_fmac_f32_e32 v57, v50, v31
	v_fmac_f32_e32 v56, v51, v31
	v_pk_mul_f32 v[50:51], v[4:5], v[32:33]
	v_fmac_f32_e32 v55, v52, v31
	v_fmac_f32_e32 v54, v53, v31
	v_and_b32_sdwa v33, v30, v45 dst_sel:DWORD dst_unused:UNUSED_PAD src0_sel:WORD_1 src1_sel:DWORD
	v_and_b32_sdwa v52, v51, v45 dst_sel:DWORD dst_unused:UNUSED_PAD src0_sel:WORD_1 src1_sel:DWORD
	v_and_b32_sdwa v53, v31, v45 dst_sel:DWORD dst_unused:UNUSED_PAD src0_sel:WORD_1 src1_sel:DWORD
	v_and_b32_sdwa v32, v50, v45 dst_sel:DWORD dst_unused:UNUSED_PAD src0_sel:WORD_1 src1_sel:DWORD
	v_add3_u32 v30, v30, v33, s22
	v_add3_u32 v33, v51, v52, s22
	v_add3_u32 v31, v31, v53, s22
	ds_read_b128 v[62:65], v35 offset:5120
	s_waitcnt lgkmcnt(1)
	v_fmac_f32_e32 v61, v26, v50
	v_fmac_f32_e32 v60, v27, v50
	v_fmac_f32_e32 v59, v28, v50
	v_fmac_f32_e32 v58, v29, v50
	ds_read_b128 v[26:29], v35 offset:6144
	v_add3_u32 v32, v50, v32, s22
	v_and_b32_e32 v33, 0xffff0000, v33
	v_and_b32_e32 v31, 0xffff0000, v31
	v_or_b32_sdwa v53, v33, v32 dst_sel:DWORD dst_unused:UNUSED_PAD src0_sel:DWORD src1_sel:WORD_1
	v_or_b32_sdwa v52, v31, v30 dst_sel:DWORD dst_unused:UNUSED_PAD src0_sel:DWORD src1_sel:WORD_1
	ds_read_b128 v[30:33], v35 offset:7168
	v_pk_mul_f32 v[48:49], v[48:49], v[44:45] op_sel_hi:[1,0]
	v_pk_mul_f32 v[46:47], v[6:7], v[46:47]
	v_pk_mul_f32 v[48:49], v[8:9], v[48:49]
	s_waitcnt lgkmcnt(2)
	v_fmac_f32_e32 v57, v62, v50
	v_fmac_f32_e32 v56, v63, v50
	s_waitcnt lgkmcnt(1)
	v_fmac_f32_e32 v61, v26, v51
	v_fmac_f32_e32 v60, v27, v51
	v_and_b32_sdwa v26, v48, v45 dst_sel:DWORD dst_unused:UNUSED_PAD src0_sel:WORD_1 src1_sel:DWORD
	v_and_b32_sdwa v27, v46, v45 dst_sel:DWORD dst_unused:UNUSED_PAD src0_sel:WORD_1 src1_sel:DWORD
	s_waitcnt lgkmcnt(0)
	v_fmac_f32_e32 v57, v30, v51
	v_fmac_f32_e32 v56, v31, v51
	v_add3_u32 v30, v46, v27, s22
	v_add3_u32 v31, v48, v26, s22
	v_and_b32_sdwa v26, v49, v45 dst_sel:DWORD dst_unused:UNUSED_PAD src0_sel:WORD_1 src1_sel:DWORD
	v_and_b32_sdwa v27, v47, v45 dst_sel:DWORD dst_unused:UNUSED_PAD src0_sel:WORD_1 src1_sel:DWORD
	v_fmac_f32_e32 v55, v64, v50
	v_fmac_f32_e32 v54, v65, v50
	v_add3_u32 v26, v49, v26, s22
	v_add3_u32 v27, v47, v27, s22
	v_fmac_f32_e32 v55, v32, v51
	v_fmac_f32_e32 v54, v33, v51
	v_and_b32_e32 v32, 0xffff0000, v26
	v_and_b32_e32 v33, 0xffff0000, v27
	v_or_b32_sdwa v31, v32, v31 dst_sel:DWORD dst_unused:UNUSED_PAD src0_sel:DWORD src1_sel:WORD_1
	v_or_b32_sdwa v30, v33, v30 dst_sel:DWORD dst_unused:UNUSED_PAD src0_sel:DWORD src1_sel:WORD_1
	v_fmac_f32_e32 v59, v28, v51
	v_fmac_f32_e32 v58, v29, v51
	ds_read_b128 v[26:29], v35 offset:8192
	global_store_dwordx2 v[42:43], v[30:31], off offset:512 sc0 sc1
	ds_read_b128 v[30:33], v35 offset:9216
	v_pk_mul_f32 v[22:23], v[22:23], v[44:45] op_sel_hi:[1,0]
	v_pk_mul_f32 v[24:25], v[24:25], v[44:45] op_sel_hi:[1,0]
	s_waitcnt lgkmcnt(1)
; #define LAS __attribute__((address_space(3)))
; __device__ __forceinline__ unsigned pk2(float lo, float hi) { return f2bf(lo) | (f2bf(hi) << 16); }
; __device__ __forceinline__ void p0_prologue(const Params& P, LAS unsigned char* lds, int tid, int lane, int wave, int vcu, int G) {
;     ...
;             for (int j = 0; j < 4; ++j) {
;                 v[j] = v[j] * rstd * w4[j];
;                 v2u o; o.x = pk2(v[j].x, v[j].y); o.y = pk2(v[j].z, v[j].w); o8[64 * j] = o;
; #pragma unroll
;                 for (int e = 0; e < 4; ++e) {
;                     const f32x4 wa = *(const LAS f32x4*)(wabl + ((((j * 4 + e) * 2 + 0) * 64 + lane) << 2));
;                     const f32x4 wb = *(const LAS f32x4*)(wabl + ((((j * 4 + e) * 2 + 1) * 64 + lane) << 2));
;                     const float hv = v[j][e];
;                     part[0] += hv * wa.x; part[1] += hv * wa.y; part[2] += hv * wa.z; part[3] += hv * wa.w;
;                     part[4] += hv * wb.x; part[5] += hv * wb.y; part[6] += hv * wb.z; part[7] += hv * wb.w;
;                 }
	v_fmac_f32_e32 v61, v46, v26
	v_fmac_f32_e32 v60, v46, v27
	v_fmac_f32_e32 v59, v46, v28
	v_fmac_f32_e32 v58, v46, v29
	s_waitcnt lgkmcnt(0)
	v_fmac_f32_e32 v57, v46, v30
	ds_read_b128 v[26:29], v35 offset:10240
	v_fmac_f32_e32 v56, v46, v31
	v_fmac_f32_e32 v55, v46, v32
	v_fmac_f32_e32 v54, v46, v33
	ds_read_b128 v[30:33], v35 offset:11264
	s_waitcnt lgkmcnt(1)
	v_fmac_f32_e32 v61, v47, v26
	v_fmac_f32_e32 v60, v47, v27
	v_fmac_f32_e32 v59, v47, v28
	v_fmac_f32_e32 v58, v47, v29
	s_waitcnt lgkmcnt(0)
	v_fmac_f32_e32 v57, v47, v30
	ds_read_b128 v[26:29], v35 offset:12288
	v_fmac_f32_e32 v56, v47, v31
	v_fmac_f32_e32 v55, v47, v32
	v_fmac_f32_e32 v54, v47, v33
	ds_read_b128 v[30:33], v35 offset:13312
	s_waitcnt lgkmcnt(1)
	v_fmac_f32_e32 v61, v48, v26
	v_fmac_f32_e32 v60, v48, v27
	v_fmac_f32_e32 v59, v48, v28
	v_fmac_f32_e32 v58, v48, v29
	s_waitcnt lgkmcnt(0)
	v_fmac_f32_e32 v57, v48, v30
	ds_read_b128 v[26:29], v35 offset:14336
	v_fmac_f32_e32 v56, v48, v31
	v_fmac_f32_e32 v55, v48, v32
	v_fmac_f32_e32 v54, v48, v33
	ds_read_b128 v[30:33], v35 offset:15360
	s_waitcnt lgkmcnt(1)
	v_fmac_f32_e32 v61, v49, v26
	v_fmac_f32_e32 v60, v49, v27
	v_fmac_f32_e32 v59, v49, v28
	v_fmac_f32_e32 v58, v49, v29
	s_waitcnt lgkmcnt(0)
	v_fmac_f32_e32 v57, v49, v30
	v_fmac_f32_e32 v56, v49, v31
	v_fmac_f32_e32 v55, v49, v32
	v_fmac_f32_e32 v54, v49, v33
	v_pk_mul_f32 v[30:31], v[12:13], v[24:25]
	v_pk_mul_f32 v[32:33], v[10:11], v[22:23]
	v_and_b32_sdwa v22, v30, v45 dst_sel:DWORD dst_unused:UNUSED_PAD src0_sel:WORD_1 src1_sel:DWORD
	v_and_b32_sdwa v23, v32, v45 dst_sel:DWORD dst_unused:UNUSED_PAD src0_sel:WORD_1 src1_sel:DWORD
	v_add3_u32 v26, v32, v23, s22
	v_add3_u32 v27, v30, v22, s22
	v_and_b32_sdwa v22, v31, v45 dst_sel:DWORD dst_unused:UNUSED_PAD src0_sel:WORD_1 src1_sel:DWORD
	v_and_b32_sdwa v23, v33, v45 dst_sel:DWORD dst_unused:UNUSED_PAD src0_sel:WORD_1 src1_sel:DWORD
	v_add3_u32 v22, v31, v22, s22
	v_add3_u32 v23, v33, v23, s22
	v_and_b32_e32 v28, 0xffff0000, v22
	v_and_b32_e32 v29, 0xffff0000, v23
	v_or_b32_sdwa v27, v28, v27 dst_sel:DWORD dst_unused:UNUSED_PAD src0_sel:DWORD src1_sel:WORD_1
	v_or_b32_sdwa v26, v29, v26 dst_sel:DWORD dst_unused:UNUSED_PAD src0_sel:DWORD src1_sel:WORD_1
	ds_read_b128 v[22:25], v35 offset:16384
	global_store_dwordx2 v[42:43], v[26:27], off offset:1024 sc0 sc1
	ds_read_b128 v[26:29], v35 offset:17408
	v_pk_mul_f32 v[18:19], v[18:19], v[44:45] op_sel_hi:[1,0]
	v_pk_mul_f32 v[20:21], v[20:21], v[44:45] op_sel_hi:[1,0]
	s_waitcnt lgkmcnt(1)
	v_fmac_f32_e32 v61, v32, v22
	v_fmac_f32_e32 v60, v32, v23
	v_fmac_f32_e32 v59, v32, v24
	v_fmac_f32_e32 v58, v32, v25
	s_waitcnt lgkmcnt(0)
	v_fmac_f32_e32 v57, v32, v26
	ds_read_b128 v[22:25], v35 offset:18432
	v_fmac_f32_e32 v56, v32, v27
	v_fmac_f32_e32 v55, v32, v28
	v_fmac_f32_e32 v54, v32, v29
	ds_read_b128 v[26:29], v35 offset:19456
	s_waitcnt lgkmcnt(1)
	v_fmac_f32_e32 v61, v33, v22
	v_fmac_f32_e32 v60, v33, v23
	v_fmac_f32_e32 v59, v33, v24
	v_fmac_f32_e32 v58, v33, v25
	s_waitcnt lgkmcnt(0)
	v_fmac_f32_e32 v57, v33, v26
	ds_read_b128 v[22:25], v35 offset:20480
	v_fmac_f32_e32 v56, v33, v27
	v_fmac_f32_e32 v55, v33, v28
	v_fmac_f32_e32 v54, v33, v29
	ds_read_b128 v[26:29], v35 offset:21504
	s_waitcnt lgkmcnt(1)
	v_fmac_f32_e32 v61, v30, v22
	v_fmac_f32_e32 v60, v30, v23
	v_fmac_f32_e32 v59, v30, v24
	v_fmac_f32_e32 v58, v30, v25
	s_waitcnt lgkmcnt(0)
	v_fmac_f32_e32 v57, v30, v26
	ds_read_b128 v[22:25], v35 offset:22528
	v_fmac_f32_e32 v56, v30, v27
	v_fmac_f32_e32 v55, v30, v28
	v_fmac_f32_e32 v54, v30, v29
	ds_read_b128 v[26:29], v35 offset:23552
	s_waitcnt lgkmcnt(1)
	v_fmac_f32_e32 v61, v31, v22
	v_fmac_f32_e32 v60, v31, v23
	v_fmac_f32_e32 v59, v31, v24
	v_fmac_f32_e32 v58, v31, v25
	s_waitcnt lgkmcnt(0)
	v_fmac_f32_e32 v57, v31, v26
	v_fmac_f32_e32 v56, v31, v27
	v_fmac_f32_e32 v55, v31, v28
	v_fmac_f32_e32 v54, v31, v29
	v_pk_mul_f32 v[26:27], v[16:17], v[20:21]
	v_pk_mul_f32 v[28:29], v[14:15], v[18:19]
	v_and_b32_sdwa v18, v26, v45 dst_sel:DWORD dst_unused:UNUSED_PAD src0_sel:WORD_1 src1_sel:DWORD
	v_and_b32_sdwa v19, v28, v45 dst_sel:DWORD dst_unused:UNUSED_PAD src0_sel:WORD_1 src1_sel:DWORD
	v_add3_u32 v22, v28, v19, s22
	v_add3_u32 v23, v26, v18, s22
	v_and_b32_sdwa v18, v27, v45 dst_sel:DWORD dst_unused:UNUSED_PAD src0_sel:WORD_1 src1_sel:DWORD
	v_and_b32_sdwa v19, v29, v45 dst_sel:DWORD dst_unused:UNUSED_PAD src0_sel:WORD_1 src1_sel:DWORD
	v_add3_u32 v18, v27, v18, s22
	v_add3_u32 v19, v29, v19, s22
	v_and_b32_e32 v24, 0xffff0000, v18
	v_and_b32_e32 v25, 0xffff0000, v19
	ds_read_b128 v[18:21], v35 offset:24576
	v_or_b32_sdwa v23, v24, v23 dst_sel:DWORD dst_unused:UNUSED_PAD src0_sel:DWORD src1_sel:WORD_1
	v_or_b32_sdwa v22, v25, v22 dst_sel:DWORD dst_unused:UNUSED_PAD src0_sel:DWORD src1_sel:WORD_1
	global_store_dwordx2 v[42:43], v[22:23], off offset:1536 sc0 sc1
	ds_read_b128 v[22:25], v35 offset:25600
	s_waitcnt lgkmcnt(1)
	v_fmac_f32_e32 v61, v28, v18
	v_fmac_f32_e32 v60, v28, v19
	v_fmac_f32_e32 v59, v28, v20
	v_fmac_f32_e32 v58, v28, v21
	ds_read_b128 v[18:21], v35 offset:26624
	s_waitcnt lgkmcnt(1)
	v_fmac_f32_e32 v57, v28, v22
	v_fmac_f32_e32 v56, v28, v23
	v_fmac_f32_e32 v55, v28, v24
	v_fmac_f32_e32 v54, v28, v25
	ds_read_b128 v[22:25], v35 offset:27648
	s_waitcnt lgkmcnt(1)
	v_fmac_f32_e32 v61, v29, v18
	v_fmac_f32_e32 v60, v29, v19
	v_fmac_f32_e32 v59, v29, v20
	v_fmac_f32_e32 v58, v29, v21
	ds_read_b128 v[18:21], v35 offset:28672
	s_waitcnt lgkmcnt(1)
	v_fmac_f32_e32 v57, v29, v22
	v_fmac_f32_e32 v56, v29, v23
	v_fmac_f32_e32 v55, v29, v24
	v_fmac_f32_e32 v54, v29, v25
	ds_read_b128 v[22:25], v35 offset:29696
	s_waitcnt lgkmcnt(1)
; #define LAS __attribute__((address_space(3)))
; __device__ __forceinline__ unsigned pk2(float lo, float hi) { return f2bf(lo) | (f2bf(hi) << 16); }
; __device__ __forceinline__ void p0_prologue(const Params& P, LAS unsigned char* lds, int tid, int lane, int wave, int vcu, int G) {
;     ...
;             for (int j = 0; j < 4; ++j) {
;                 v[j] = v[j] * rstd * w4[j];
;                 v2u o; o.x = pk2(v[j].x, v[j].y); o.y = pk2(v[j].z, v[j].w); o8[64 * j] = o;
; #pragma unroll
;                 for (int e = 0; e < 4; ++e) {
;                     const f32x4 wa = *(const LAS f32x4*)(wabl + ((((j * 4 + e) * 2 + 0) * 64 + lane) << 2));
;                     const f32x4 wb = *(const LAS f32x4*)(wabl + ((((j * 4 + e) * 2 + 1) * 64 + lane) << 2));
;                     const float hv = v[j][e];
;                     part[0] += hv * wa.x; part[1] += hv * wa.y; part[2] += hv * wa.z; part[3] += hv * wa.w;
;                     part[4] += hv * wb.x; part[5] += hv * wb.y; part[6] += hv * wb.z; part[7] += hv * wb.w;
;                 }
;             }
; #pragma unroll
;             for (int c = 0; c < 8; ++c) part[c] = wave_sum(part[c]);
;             float o = part[0];
; #pragma unroll
;             for (int c = 1; c < 8; ++c) o = (lane == c) ? part[c] : o;
;             if (lane < 8) AB[(size_t)m * 8 + lane] = o;
	v_fmac_f32_e32 v61, v26, v18
	v_fmac_f32_e32 v60, v26, v19
	v_fmac_f32_e32 v59, v26, v20
	v_fmac_f32_e32 v58, v26, v21
	ds_read_b128 v[18:21], v35 offset:30720
	s_waitcnt lgkmcnt(1)
	v_fmac_f32_e32 v57, v26, v22
	v_fmac_f32_e32 v56, v26, v23
	v_fmac_f32_e32 v55, v26, v24
	v_fmac_f32_e32 v54, v26, v25
	ds_read_b128 v[22:25], v35 offset:31744
	s_waitcnt lgkmcnt(1)
	v_fmac_f32_e32 v61, v27, v18
	v_fmac_f32_e32 v60, v27, v19
	v_fmac_f32_e32 v59, v27, v20
	v_add_f32_dpp v18, v61, v61 quad_perm:[1,0,3,2] row_mask:0xf bank_mask:0xf bound_ctrl:1
	v_fmac_f32_e32 v58, v27, v21
	s_waitcnt lgkmcnt(0)
	v_fmac_f32_e32 v57, v27, v22
	v_add_f32_dpp v18, v18, v18 quad_perm:[2,3,0,1] row_mask:0xf bank_mask:0xf bound_ctrl:1
	v_fmac_f32_e32 v56, v27, v23
	v_fmac_f32_e32 v55, v27, v24
	v_add_f32_dpp v18, v18, v18 row_half_mirror row_mask:0xf bank_mask:0xf bound_ctrl:1
	v_fmac_f32_e32 v54, v27, v25
	global_store_dwordx2 v[42:43], v[52:53], off sc0 sc1
	v_add_f32_dpp v18, v18, v18 row_mirror row_mask:0xf bank_mask:0xf bound_ctrl:1
	v_mov_b32_e32 v19, v18
	s_nop 1
	v_permlane16_swap_b32_e32 v18, v19
	v_add_f32 v18, v18, v19
	s_nop 1
	s_nop 0
	v_mov_b32_e32 v19, v18
	s_nop 1
	v_permlane32_swap_b32_e32 v18, v19
	v_add_f32 v18, v18, v19
	s_nop 1
	v_add_f32_dpp v19, v60, v60 quad_perm:[1,0,3,2] row_mask:0xf bank_mask:0xf bound_ctrl:1
	s_nop 1
	v_add_f32_dpp v19, v19, v19 quad_perm:[2,3,0,1] row_mask:0xf bank_mask:0xf bound_ctrl:1
	s_nop 1
	v_add_f32_dpp v19, v19, v19 row_half_mirror row_mask:0xf bank_mask:0xf bound_ctrl:1
	s_nop 1
	v_add_f32_dpp v19, v19, v19 row_mirror row_mask:0xf bank_mask:0xf bound_ctrl:1
	v_mov_b32_e32 v20, v19
	s_nop 1
	v_permlane16_swap_b32_e32 v19, v20
	v_add_f32 v19, v19, v20
	s_nop 1
	s_nop 0
	v_mov_b32_e32 v20, v19
	s_nop 1
	v_permlane32_swap_b32_e32 v19, v20
	v_add_f32 v19, v19, v20
	s_nop 1
	v_add_f32_dpp v20, v59, v59 quad_perm:[1,0,3,2] row_mask:0xf bank_mask:0xf bound_ctrl:1
	s_nop 1
	v_add_f32_dpp v20, v20, v20 quad_perm:[2,3,0,1] row_mask:0xf bank_mask:0xf bound_ctrl:1
	s_nop 1
	v_add_f32_dpp v20, v20, v20 row_half_mirror row_mask:0xf bank_mask:0xf bound_ctrl:1
	s_nop 1
	v_add_f32_dpp v20, v20, v20 row_mirror row_mask:0xf bank_mask:0xf bound_ctrl:1
	v_mov_b32_e32 v21, v20
	s_nop 1
	v_permlane16_swap_b32_e32 v20, v21
	v_add_f32 v20, v20, v21
	s_nop 1
	s_nop 0
	v_mov_b32_e32 v21, v20
	s_nop 1
	v_permlane32_swap_b32_e32 v20, v21
	v_add_f32 v20, v20, v21
	s_nop 1
	v_add_f32_dpp v21, v58, v58 quad_perm:[1,0,3,2] row_mask:0xf bank_mask:0xf bound_ctrl:1
	s_nop 1
	v_add_f32_dpp v21, v21, v21 quad_perm:[2,3,0,1] row_mask:0xf bank_mask:0xf bound_ctrl:1
	s_nop 1
	v_add_f32_dpp v21, v21, v21 row_half_mirror row_mask:0xf bank_mask:0xf bound_ctrl:1
	s_nop 1
	v_add_f32_dpp v21, v21, v21 row_mirror row_mask:0xf bank_mask:0xf bound_ctrl:1
	v_mov_b32_e32 v22, v21
	s_nop 1
	v_permlane16_swap_b32_e32 v21, v22
	v_add_f32 v21, v21, v22
	s_nop 1
	s_nop 0
	v_mov_b32_e32 v22, v21
	s_nop 1
	v_permlane32_swap_b32_e32 v21, v22
	v_add_f32 v21, v21, v22
	s_nop 1
	v_add_f32_dpp v22, v57, v57 quad_perm:[1,0,3,2] row_mask:0xf bank_mask:0xf bound_ctrl:1
	s_nop 1
	v_add_f32_dpp v22, v22, v22 quad_perm:[2,3,0,1] row_mask:0xf bank_mask:0xf bound_ctrl:1
	s_nop 1
	v_add_f32_dpp v22, v22, v22 row_half_mirror row_mask:0xf bank_mask:0xf bound_ctrl:1
	s_nop 1
	v_add_f32_dpp v22, v22, v22 row_mirror row_mask:0xf bank_mask:0xf bound_ctrl:1
	v_mov_b32_e32 v23, v22
	s_nop 1
	v_permlane16_swap_b32_e32 v22, v23
	v_add_f32 v22, v22, v23
	s_nop 1
	s_nop 0
	v_mov_b32_e32 v23, v22
	s_nop 1
	v_permlane32_swap_b32_e32 v22, v23
	v_add_f32 v22, v22, v23
	s_nop 1
	v_add_f32_dpp v23, v56, v56 quad_perm:[1,0,3,2] row_mask:0xf bank_mask:0xf bound_ctrl:1
	s_nop 1
	v_add_f32_dpp v23, v23, v23 quad_perm:[2,3,0,1] row_mask:0xf bank_mask:0xf bound_ctrl:1
	s_nop 1
	v_add_f32_dpp v23, v23, v23 row_half_mirror row_mask:0xf bank_mask:0xf bound_ctrl:1
	s_nop 1
	v_add_f32_dpp v23, v23, v23 row_mirror row_mask:0xf bank_mask:0xf bound_ctrl:1
	v_mov_b32_e32 v24, v23
	s_nop 1
	v_permlane16_swap_b32_e32 v23, v24
	v_add_f32 v23, v23, v24
	s_nop 1
	s_nop 0
	v_mov_b32_e32 v24, v23
	s_nop 1
	v_permlane32_swap_b32_e32 v23, v24
	v_add_f32 v23, v23, v24
	s_nop 1
	v_add_f32_dpp v24, v55, v55 quad_perm:[1,0,3,2] row_mask:0xf bank_mask:0xf bound_ctrl:1
	s_nop 1
	v_add_f32_dpp v24, v24, v24 quad_perm:[2,3,0,1] row_mask:0xf bank_mask:0xf bound_ctrl:1
	s_nop 1
	v_add_f32_dpp v24, v24, v24 row_half_mirror row_mask:0xf bank_mask:0xf bound_ctrl:1
	s_nop 1
	v_add_f32_dpp v24, v24, v24 row_mirror row_mask:0xf bank_mask:0xf bound_ctrl:1
	v_mov_b32_e32 v25, v24
	s_nop 1
	v_permlane16_swap_b32_e32 v24, v25
	v_add_f32 v24, v24, v25
	s_nop 1
	s_nop 0
	v_mov_b32_e32 v25, v24
	s_nop 1
	v_permlane32_swap_b32_e32 v24, v25
	v_add_f32 v24, v24, v25
	s_nop 1
	v_add_f32_dpp v25, v54, v54 quad_perm:[1,0,3,2] row_mask:0xf bank_mask:0xf bound_ctrl:1
	s_nop 1
	v_add_f32_dpp v25, v25, v25 quad_perm:[2,3,0,1] row_mask:0xf bank_mask:0xf bound_ctrl:1
	s_nop 1
	v_add_f32_dpp v25, v25, v25 row_half_mirror row_mask:0xf bank_mask:0xf bound_ctrl:1
	s_nop 1
	v_add_f32_dpp v25, v25, v25 row_mirror row_mask:0xf bank_mask:0xf bound_ctrl:1
	v_mov_b32_e32 v26, v25
	s_nop 1
	v_permlane16_swap_b32_e32 v25, v26
	v_add_f32 v25, v25, v26
	s_nop 1
	s_nop 0
	v_mov_b32_e32 v26, v25
	s_nop 1
	v_permlane32_swap_b32_e32 v25, v26
	v_add_f32 v25, v25, v26
	s_and_saveexec_b64 s[0:1], s[10:11]
	s_cbranch_execz .LBB0_17
	v_cndmask_b32_e64 v18, v18, v19, s[8:9]
	v_cndmask_b32_e64 v18, v18, v20, s[16:17]
	v_cndmask_b32_e64 v18, v18, v21, s[6:7]
	v_cndmask_b32_e64 v18, v18, v22, s[14:15]
	v_cndmask_b32_e64 v18, v18, v23, s[4:5]
	v_cndmask_b32_e64 v18, v18, v24, s[12:13]
	v_cndmask_b32_e32 v20, v18, v25, vcc
	v_lshl_add_u64 v[18:19], s[24:25], 0, v[36:37]
	global_store_dword v[18:19], v20, off
	s_branch .LBB0_17

; __device__ __forceinline__ unsigned pk2(float lo, float hi) { return f2bf(lo) | (f2bf(hi) << 16); }
; __device__ __forceinline__ void p0_prologue(const Params& P, LAS unsigned char* lds, int tid, int lane, int wave, int vcu, int G) {
;     ...
;         for (int m = gw; m < 512; m += NGW) {
;             const f32x4* xr = (const f32x4*)(P.mem + (size_t)m * D) + lane;
;             f32x4 v[4]; float s = 0.f;
; #pragma unroll
;             for (int j = 0; j < 4; ++j) { v[j] = xr[64 * j]; s += (v[j].x * v[j].x + v[j].y * v[j].y) + (v[j].z * v[j].z + v[j].w * v[j].w); }
;             const float rstd = rsqrtf(wave_sum(s) * (1.0f / D) + 1e-6f);
;             v2u* o8 = (v2u*)(MEMN + (size_t)m * D) + lane;
; #pragma unroll
;             for (int j = 0; j < 4; ++j) { const f32x4 w = ((const f32x4*)P.norm_mem_w)[64 * j + lane]; const f32x4 y = v[j] * rstd * w;
;                 v2u o; o.x = pk2(y.x, y.y); o.y = pk2(y.z, y.w); o8[64 * j] = o; }
;         }
.LBB0_22:
	global_load_dwordx4 v[8:11], v[6:7], off offset:-3072
	global_load_dwordx4 v[12:15], v[6:7], off offset:-2048
	global_load_dwordx4 v[16:19], v[6:7], off offset:-1024
	global_load_dwordx4 v[20:23], v[6:7], off
	global_load_dwordx4 v[24:27], v[2:3], off
	s_add_i32 s9, s9, s54
	v_lshl_add_u64 v[6:7], v[6:7], 0, s[4:5]
	s_cmpk_gt_i32 s9, 0x1ff
	s_waitcnt vmcnt(4)
	v_mul_f32_e32 v28, v9, v9
	v_mul_f32_e32 v29, v11, v11
	s_waitcnt vmcnt(3)
	v_mul_f32_e32 v30, v13, v13
	v_mul_f32_e32 v31, v15, v15
	s_waitcnt vmcnt(2)
	v_mul_f32_e32 v32, v17, v17
	v_mul_f32_e32 v33, v19, v19
	v_fmac_f32_e32 v28, v8, v8
	v_fmac_f32_e32 v29, v10, v10
	v_fmac_f32_e32 v30, v12, v12
	v_fmac_f32_e32 v31, v14, v14
	s_waitcnt vmcnt(1)
	v_mul_f32_e32 v34, v21, v21
	v_mul_f32_e32 v35, v23, v23
	v_fmac_f32_e32 v32, v16, v16
	v_fmac_f32_e32 v33, v18, v18
	v_add_f32_e32 v28, v28, v29
	v_add_f32_e32 v29, v30, v31
	v_fmac_f32_e32 v34, v20, v20
	v_fmac_f32_e32 v35, v22, v22
	v_add_f32_e32 v30, v32, v33
	v_add_f32_e32 v28, v28, v29
	v_add_f32_e32 v31, v34, v35
	v_add_f32_e32 v28, v28, v30
	v_add_f32_e32 v28, v28, v31
	s_nop 1
	v_add_f32_dpp v28, v28, v28 quad_perm:[1,0,3,2] row_mask:0xf bank_mask:0xf bound_ctrl:1
	s_nop 1
	v_add_f32_dpp v28, v28, v28 quad_perm:[2,3,0,1] row_mask:0xf bank_mask:0xf bound_ctrl:1
	s_nop 1
	v_add_f32_dpp v28, v28, v28 row_half_mirror row_mask:0xf bank_mask:0xf bound_ctrl:1
	s_nop 1
	v_add_f32_dpp v28, v28, v28 row_mirror row_mask:0xf bank_mask:0xf bound_ctrl:1
	v_mov_b32_e32 v29, v28
	s_nop 1
	v_permlane16_swap_b32_e32 v28, v29
	v_add_f32 v28, v28, v29
	s_nop 1
	s_nop 0
	v_mov_b32_e32 v29, v28
	s_nop 1
	v_permlane32_swap_b32_e32 v28, v29
	v_add_f32 v28, v28, v29
	s_nop 0
	v_fmamk_f32 v28, v28, 0x3a800000, v1
	v_mul_f32_e32 v29, 0x4b800000, v28
	v_cmp_gt_f32_e32 vcc, s6, v28
	s_nop 1
	v_cndmask_b32_e32 v28, v28, v29, vcc
	v_rsq_f32_e32 v28, v28
	s_nop 0
	v_mul_f32_e32 v29, 0x45800000, v28
	v_cndmask_b32_e32 v28, v28, v29, vcc
	v_pk_mul_f32 v[8:9], v[8:9], v[28:29] op_sel_hi:[1,0]
	v_pk_mul_f32 v[10:11], v[10:11], v[28:29] op_sel_hi:[1,0]
	s_waitcnt vmcnt(0)
	v_pk_mul_f32 v[8:9], v[24:25], v[8:9]
	v_pk_mul_f32 v[10:11], v[26:27], v[10:11]
	v_bfe_u32 v24, v8, 16, 1
	v_bfe_u32 v26, v10, 16, 1
	v_bfe_u32 v25, v9, 16, 1
	v_bfe_u32 v27, v11, 16, 1
	v_add3_u32 v8, v8, v24, s7
	v_add3_u32 v10, v10, v26, s7
	v_add3_u32 v9, v9, v25, s7
	v_add3_u32 v11, v11, v27, s7
	v_lshrrev_b32_e32 v8, 16, v8
	v_lshrrev_b32_e32 v10, 16, v10
	v_and_or_b32 v8, v9, s8, v8
	v_and_or_b32 v9, v11, s8, v10
	global_store_dwordx2 v[4:5], v[8:9], off sc0 sc1
	global_load_dwordx4 v[8:11], v[2:3], off offset:1024
	v_pk_mul_f32 v[12:13], v[12:13], v[28:29] op_sel_hi:[1,0]
	v_pk_mul_f32 v[14:15], v[14:15], v[28:29] op_sel_hi:[1,0]
	s_waitcnt vmcnt(0)
	v_pk_mul_f32 v[8:9], v[8:9], v[12:13]
	v_pk_mul_f32 v[10:11], v[10:11], v[14:15]
	v_bfe_u32 v12, v8, 16, 1
	v_bfe_u32 v14, v10, 16, 1
	v_bfe_u32 v13, v9, 16, 1
	v_bfe_u32 v15, v11, 16, 1
	v_add3_u32 v8, v8, v12, s7
	v_add3_u32 v10, v10, v14, s7
	v_add3_u32 v9, v9, v13, s7
	v_add3_u32 v11, v11, v15, s7
	v_lshrrev_b32_e32 v8, 16, v8
	v_lshrrev_b32_e32 v10, 16, v10
	v_and_or_b32 v8, v9, s8, v8
	v_and_or_b32 v9, v11, s8, v10
	global_store_dwordx2 v[4:5], v[8:9], off offset:512 sc0 sc1
	global_load_dwordx4 v[8:11], v[2:3], off offset:2048
	v_pk_mul_f32 v[12:13], v[16:17], v[28:29] op_sel_hi:[1,0]
	v_pk_mul_f32 v[14:15], v[18:19], v[28:29] op_sel_hi:[1,0]
	s_waitcnt vmcnt(0)
	v_pk_mul_f32 v[8:9], v[8:9], v[12:13]
	v_pk_mul_f32 v[10:11], v[10:11], v[14:15]
	v_bfe_u32 v12, v8, 16, 1
	v_bfe_u32 v14, v10, 16, 1
	v_bfe_u32 v13, v9, 16, 1
	v_bfe_u32 v15, v11, 16, 1
	v_add3_u32 v8, v8, v12, s7
	v_add3_u32 v10, v10, v14, s7
	v_add3_u32 v9, v9, v13, s7
	v_add3_u32 v11, v11, v15, s7
	v_lshrrev_b32_e32 v8, 16, v8
	v_lshrrev_b32_e32 v10, 16, v10
	v_and_or_b32 v8, v9, s8, v8
	v_and_or_b32 v9, v11, s8, v10
	global_store_dwordx2 v[4:5], v[8:9], off offset:1024 sc0 sc1
	global_load_dwordx4 v[8:11], v[2:3], off offset:3072
	v_pk_mul_f32 v[12:13], v[20:21], v[28:29] op_sel_hi:[1,0]
	v_pk_mul_f32 v[14:15], v[22:23], v[28:29] op_sel_hi:[1,0]
	s_waitcnt vmcnt(0)
	v_pk_mul_f32 v[8:9], v[8:9], v[12:13]
	v_pk_mul_f32 v[10:11], v[10:11], v[14:15]
	v_bfe_u32 v12, v8, 16, 1
	v_bfe_u32 v14, v10, 16, 1
	v_bfe_u32 v13, v9, 16, 1
	v_bfe_u32 v15, v11, 16, 1
	v_add3_u32 v8, v8, v12, s7
	v_add3_u32 v10, v10, v14, s7
	v_add3_u32 v9, v9, v13, s7
	v_add3_u32 v11, v11, v15, s7
	v_lshrrev_b32_e32 v8, 16, v8
	v_lshrrev_b32_e32 v10, 16, v10
	v_and_or_b32 v8, v9, s8, v8
	v_and_or_b32 v9, v11, s8, v10
	global_store_dwordx2 v[4:5], v[8:9], off offset:1536 sc0 sc1
	v_lshl_add_u64 v[4:5], v[4:5], 0, s[0:1]
	s_cbranch_scc0 .LBB0_22

; #define LAS __attribute__((address_space(3)))
; #define LDS_WAIT() asm volatile("s_waitcnt lgkmcnt(0)" ::: "memory")
; __device__ __forceinline__ void p0_transpose_item(const float* W, int K, int ldw, int c0, int nblk, bf16* WT, int row_off, const float* ks, LAS float* scr, int item, int lane) {
;     const int kb = item / nblk, nb = item % nblk, k0 = 64 * kb, n0 = 32 * nb;
; #pragma unroll 8
;     for (int i = 0; i < 32; ++i) { const int kk = 2 * i + (lane >> 5); float v = W[(size_t)(k0 + kk) * ldw + c0 + n0 + (lane & 31)]; if (ks) v *= ks[k0 + kk]; scr[kk * 33 + (lane & 31)] = v; }
;     LDS_WAIT(); asm volatile("" ::: "memory");
.LBB0_32:
	s_lshl_b32 s13, s0, 1
	s_lshl_b32 s14, s7, 1
	v_or_b32_e32 v6, s14, v24
	s_add_i32 s16, s13, 4
	s_add_i32 s17, s14, 4
	v_mov_b32_e32 v33, v7
	s_add_i32 s19, s14, 8
	v_lshlrev_b64 v[46:47], 13, v[6:7]
	v_or_b32_e32 v32, s16, v3
	v_or_b32_e32 v6, s17, v24
	v_mov_b32_e32 v31, v7
	v_or_b32_e32 v30, s13, v3
	s_add_i32 s23, s14, 12
	v_lshlrev_b64 v[32:33], 13, v[32:33]
	v_lshlrev_b64 v[48:49], 13, v[6:7]
	v_or_b32_e32 v6, s19, v24
	s_add_i32 s18, s13, 8
	s_add_i32 s22, s13, 12
	s_add_i32 s28, s14, 16
	v_lshlrev_b64 v[30:31], 13, v[30:31]
	v_lshl_add_u64 v[46:47], v[22:23], 0, v[46:47]
	v_lshl_add_u64 v[32:33], v[22:23], 0, v[32:33]
	v_lshlrev_b64 v[50:51], 13, v[6:7]
	v_or_b32_e32 v6, s23, v24
	v_mov_b32_e32 v35, v7
	v_mov_b32_e32 v37, v7
	s_add_i32 s30, s14, 20
	v_or_b32_e32 v34, s18, v3
	v_or_b32_e32 v36, s22, v3
	v_lshl_add_u64 v[30:31], v[22:23], 0, v[30:31]
	v_lshl_add_u64 v[48:49], v[22:23], 0, v[48:49]
	global_load_dword v62, v[46:47], off
	global_load_dword v63, v[30:31], off
	global_load_dword v64, v[48:49], off
	global_load_dword v65, v[32:33], off
	v_lshlrev_b64 v[32:33], 13, v[6:7]
	v_or_b32_e32 v6, s28, v24
	s_add_i32 s27, s13, 16
	s_add_i32 s29, s13, 20
	s_add_i32 s33, s14, 24
	v_lshlrev_b64 v[34:35], 13, v[34:35]
	v_lshlrev_b64 v[36:37], 13, v[36:37]
	v_lshl_add_u64 v[30:31], v[22:23], 0, v[50:51]
	v_lshl_add_u64 v[32:33], v[22:23], 0, v[32:33]
	v_lshlrev_b64 v[46:47], 13, v[6:7]
	v_or_b32_e32 v6, s30, v24
	v_mov_b32_e32 v39, v7
	v_mov_b32_e32 v41, v7
	s_add_i32 s31, s13, 24
	s_add_i32 s34, s13, 28
	s_add_i32 s35, s14, 28
	v_or_b32_e32 v38, s27, v3
	v_or_b32_e32 v40, s29, v3
	v_lshl_add_u64 v[34:35], v[22:23], 0, v[34:35]
	v_lshl_add_u64 v[36:37], v[22:23], 0, v[36:37]
	global_load_dword v66, v[30:31], off
	global_load_dword v67, v[34:35], off
	global_load_dword v68, v[32:33], off
	global_load_dword v69, v[36:37], off
	v_lshlrev_b64 v[32:33], 13, v[6:7]
	v_or_b32_e32 v6, s33, v24
	v_mov_b32_e32 v43, v7
	v_mov_b32_e32 v45, v7
	v_or_b32_e32 v42, s31, v3
	v_or_b32_e32 v44, s34, v3
	v_lshlrev_b64 v[38:39], 13, v[38:39]
	v_lshlrev_b64 v[40:41], 13, v[40:41]
	v_lshl_add_u64 v[30:31], v[22:23], 0, v[46:47]
	v_lshl_add_u64 v[32:33], v[22:23], 0, v[32:33]
	v_lshlrev_b64 v[34:35], 13, v[6:7]
	v_or_b32_e32 v6, s35, v24
	v_lshlrev_b64 v[42:43], 13, v[42:43]
	v_lshlrev_b64 v[44:45], 13, v[44:45]
	v_lshl_add_u64 v[38:39], v[22:23], 0, v[38:39]
	v_lshl_add_u64 v[40:41], v[22:23], 0, v[40:41]
	global_load_dword v70, v[30:31], off
	global_load_dword v71, v[38:39], off
	global_load_dword v72, v[32:33], off
	global_load_dword v73, v[40:41], off
	v_lshl_add_u64 v[30:31], v[22:23], 0, v[34:35]
	v_lshlrev_b64 v[32:33], 13, v[6:7]
	v_lshl_add_u64 v[42:43], v[22:23], 0, v[42:43]
	v_lshl_add_u64 v[44:45], v[22:23], 0, v[44:45]
	v_lshl_add_u64 v[32:33], v[22:23], 0, v[32:33]
	global_load_dword v6, v[30:31], off
	global_load_dword v74, v[42:43], off
	global_load_dword v75, v[32:33], off
	global_load_dword v76, v[44:45], off
	v_or_b32_e32 v32, s13, v1
	v_or_b32_e32 v30, s14, v2
	s_add_i32 s7, s7, 16
	s_add_i32 s0, s0, 16
	s_add_i32 s12, s12, -16
	v_mad_u64_u32 v[30:31], s[14:15], v30, s8, v[4:5]
	v_mad_u64_u32 v[32:33], s[14:15], v32, s8, v[4:5]
	v_or_b32_e32 v31, s16, v1
	v_or_b32_e32 v33, s17, v2
	v_or_b32_e32 v40, s18, v1
	v_or_b32_e32 v38, s19, v2
	v_or_b32_e32 v44, s22, v1
	v_or_b32_e32 v42, s23, v2
	v_or_b32_e32 v48, s27, v1
	v_or_b32_e32 v46, s28, v2
	v_or_b32_e32 v52, s29, v1
	v_or_b32_e32 v50, s30, v2
	v_or_b32_e32 v56, s31, v1
	v_or_b32_e32 v54, s33, v2
	v_or_b32_e32 v60, s34, v1
	v_or_b32_e32 v58, s35, v2
	s_cmp_lg_u32 s12, 0
	v_mad_u64_u32 v[34:35], s[14:15], v33, s8, v[4:5]
	v_mad_u64_u32 v[36:37], s[14:15], v31, s8, v[4:5]
	v_mad_u64_u32 v[38:39], s[14:15], v38, s8, v[4:5]
	v_mad_u64_u32 v[40:41], s[14:15], v40, s8, v[4:5]
	v_mad_u64_u32 v[42:43], s[14:15], v42, s8, v[4:5]
	v_mad_u64_u32 v[44:45], s[14:15], v44, s8, v[4:5]
	v_mad_u64_u32 v[46:47], s[14:15], v46, s8, v[4:5]
	v_mad_u64_u32 v[48:49], s[14:15], v48, s8, v[4:5]
	v_mad_u64_u32 v[50:51], s[14:15], v50, s8, v[4:5]
	v_mad_u64_u32 v[52:53], s[14:15], v52, s8, v[4:5]
	v_mad_u64_u32 v[54:55], s[14:15], v54, s8, v[4:5]
	v_mad_u64_u32 v[56:57], s[14:15], v56, s8, v[4:5]
	v_mad_u64_u32 v[58:59], s[14:15], v58, s8, v[4:5]
	v_mad_u64_u32 v[60:61], s[14:15], v60, s8, v[4:5]
	s_waitcnt vmcnt(15)
	ds_write_b32 v30, v62
	s_waitcnt vmcnt(14)
	ds_write_b32 v32, v63
	s_waitcnt vmcnt(13)
	ds_write_b32 v34, v64
	s_waitcnt vmcnt(12)
	ds_write_b32 v36, v65
	s_waitcnt vmcnt(11)
	ds_write_b32 v38, v66
	s_waitcnt vmcnt(10)
	ds_write_b32 v40, v67
	s_waitcnt vmcnt(9)
	ds_write_b32 v42, v68
	s_waitcnt vmcnt(8)
	ds_write_b32 v44, v69
	s_waitcnt vmcnt(7)
	ds_write_b32 v46, v70
	s_waitcnt vmcnt(6)
	ds_write_b32 v48, v71
	s_waitcnt vmcnt(5)
	ds_write_b32 v50, v72
	s_waitcnt vmcnt(4)
	ds_write_b32 v52, v73
	s_waitcnt vmcnt(3)
	ds_write_b32 v54, v6
	s_waitcnt vmcnt(2)
	ds_write_b32 v56, v74
	s_waitcnt vmcnt(1)
	ds_write_b32 v58, v75
	s_waitcnt vmcnt(0)
	ds_write_b32 v60, v76
	s_cbranch_scc1 .LBB0_32
; #define GAS __attribute__((address_space(1)))
; #define LAS __attribute__((address_space(3)))
; #define LDS_WAIT() asm volatile("s_waitcnt lgkmcnt(0)" ::: "memory")
; __device__ __forceinline__ unsigned pk2(float lo, float hi) { return f2bf(lo) | (f2bf(hi) << 16); }
; __device__ __forceinline__ void p0_transpose_item(const float* W, int K, int ldw, int c0, int nblk, bf16* WT, int row_off, const float* ks, LAS float* scr, int item, int lane) {
;     ...
;     const int c = lane & 7;
; #pragma unroll
;     for (int j = 0; j < 4; ++j) { const int n = (lane >> 3) + 8 * j; const LAS float* s = scr + (8 * c) * 33 + n;
;         v4u o; o.x = pk2(s[0 * 33], s[1 * 33]); o.y = pk2(s[2 * 33], s[3 * 33]); o.z = pk2(s[4 * 33], s[5 * 33]); o.w = pk2(s[6 * 33], s[7 * 33]);
;         *(GAS v4u*)(WT + (size_t)(row_off + n0 + n) * K + k0 + 8 * c) = o; }
;     LDS_WAIT(); asm volatile("" ::: "memory");
	s_waitcnt lgkmcnt(0)
	ds_read2_b32 v[22:23], v26 offset1:8
	ds_read2_b32 v[36:37], v26 offset0:33 offset1:41
	ds_read2_b32 v[38:39], v26 offset0:66 offset1:74
	ds_read2_b32 v[40:41], v26 offset0:99 offset1:107
	ds_read2_b32 v[42:43], v26 offset0:132 offset1:140
	ds_read2_b32 v[44:45], v26 offset0:165 offset1:173
	s_waitcnt lgkmcnt(5)
	v_bfe_u32 v3, v22, 16, 1
	v_add3_u32 v3, v22, v3, s9
	s_waitcnt lgkmcnt(4)
	v_bfe_u32 v6, v36, 16, 1
	v_lshrrev_b32_e32 v3, 16, v3
	v_add3_u32 v6, v36, v6, s9
	v_and_or_b32 v30, v6, s10, v3
	s_waitcnt lgkmcnt(3)
	v_bfe_u32 v3, v38, 16, 1
	v_add3_u32 v3, v38, v3, s9
	s_waitcnt lgkmcnt(2)
	v_bfe_u32 v6, v40, 16, 1
	ds_read2_b32 v[46:47], v26 offset0:198 offset1:206
	v_lshrrev_b32_e32 v3, 16, v3
	v_add3_u32 v6, v40, v6, s9
	ds_read2_b32 v[48:49], v26 offset0:231 offset1:239
	v_and_or_b32 v31, v6, s10, v3
	s_waitcnt lgkmcnt(3)
	v_bfe_u32 v3, v42, 16, 1
	v_add3_u32 v3, v42, v3, s9
	s_waitcnt lgkmcnt(2)
	v_bfe_u32 v6, v44, 16, 1
	v_lshrrev_b32_e32 v3, 16, v3
	v_add3_u32 v6, v44, v6, s9
	v_and_or_b32 v32, v6, s10, v3
	s_waitcnt lgkmcnt(1)
	v_bfe_u32 v3, v46, 16, 1
	v_add3_u32 v3, v46, v3, s9
	s_waitcnt lgkmcnt(0)
	v_bfe_u32 v6, v48, 16, 1
	v_lshrrev_b32_e32 v3, 16, v3
	v_add3_u32 v6, v48, v6, s9
	s_lshl_b32 s0, s5, 1
	v_and_or_b32 v33, v6, s10, v3
	v_or_b32_e32 v3, s4, v5
	v_lshl_add_u64 v[34:35], v[8:9], 0, s[0:1]
	v_lshlrev_b32_e32 v6, 11, v3
	v_bfe_u32 v3, v23, 16, 1
	v_lshl_add_u64 v[50:51], v[34:35], 0, v[6:7]
	v_add3_u32 v3, v23, v3, s9
	v_bfe_u32 v6, v37, 16, 1
	v_lshrrev_b32_e32 v3, 16, v3
	v_add3_u32 v6, v37, v6, s9
	global_store_dwordx4 v[50:51], v[30:33], off sc0 sc1
	ds_read2_b32 v[22:23], v26 offset0:16 offset1:24
	s_nop 0
	v_and_or_b32 v30, v6, s10, v3
	v_bfe_u32 v3, v39, 16, 1
	v_add3_u32 v3, v39, v3, s9
	v_bfe_u32 v6, v41, 16, 1
	v_lshrrev_b32_e32 v3, 16, v3
	v_add3_u32 v6, v41, v6, s9
	v_and_or_b32 v31, v6, s10, v3
	v_bfe_u32 v3, v43, 16, 1
	v_add3_u32 v3, v43, v3, s9
	v_bfe_u32 v6, v45, 16, 1
	v_lshrrev_b32_e32 v3, 16, v3
	v_add3_u32 v6, v45, v6, s9
	v_and_or_b32 v32, v6, s10, v3
	v_bfe_u32 v3, v47, 16, 1
	v_add3_u32 v3, v47, v3, s9
	v_bfe_u32 v6, v49, 16, 1
	v_lshrrev_b32_e32 v3, 16, v3
	v_add3_u32 v6, v49, v6, s9
	v_and_or_b32 v33, v6, s10, v3
	v_or_b32_e32 v3, s4, v27
	v_lshlrev_b32_e32 v6, 11, v3
	v_lshl_add_u64 v[36:37], v[34:35], 0, v[6:7]
	global_store_dwordx4 v[36:37], v[30:33], off sc0 sc1
	ds_read2_b32 v[36:37], v26 offset0:49 offset1:57
	ds_read2_b32 v[38:39], v26 offset0:82 offset1:90
	ds_read2_b32 v[40:41], v26 offset0:115 offset1:123
	s_waitcnt lgkmcnt(3)
	v_bfe_u32 v3, v22, 16, 1
	v_add3_u32 v3, v22, v3, s9
	s_waitcnt lgkmcnt(2)
	v_bfe_u32 v6, v36, 16, 1
	ds_read2_b32 v[42:43], v26 offset0:148 offset1:156
	v_lshrrev_b32_e32 v3, 16, v3
	v_add3_u32 v6, v36, v6, s9
	ds_read2_b32 v[44:45], v26 offset0:181 offset1:189
	v_and_or_b32 v30, v6, s10, v3
	s_waitcnt lgkmcnt(3)
	v_bfe_u32 v3, v38, 16, 1
	v_add3_u32 v3, v38, v3, s9
	s_waitcnt lgkmcnt(2)
	v_bfe_u32 v6, v40, 16, 1
	ds_read2_b32 v[46:47], v26 offset0:214 offset1:222
	v_lshrrev_b32_e32 v3, 16, v3
	v_add3_u32 v6, v40, v6, s9
	ds_read2_b32 v[48:49], v26 offset0:247 offset1:255
	v_and_or_b32 v31, v6, s10, v3
	s_waitcnt lgkmcnt(3)
	v_bfe_u32 v3, v42, 16, 1
	v_add3_u32 v3, v42, v3, s9
	s_waitcnt lgkmcnt(2)
	v_bfe_u32 v6, v44, 16, 1
	v_lshrrev_b32_e32 v3, 16, v3
	v_add3_u32 v6, v44, v6, s9
	v_and_or_b32 v32, v6, s10, v3
	s_waitcnt lgkmcnt(1)
	v_bfe_u32 v3, v46, 16, 1
	v_add3_u32 v3, v46, v3, s9
	s_waitcnt lgkmcnt(0)
	v_bfe_u32 v6, v48, 16, 1
	v_lshrrev_b32_e32 v3, 16, v3
	v_add3_u32 v6, v48, v6, s9
	v_and_or_b32 v33, v6, s10, v3
	v_or_b32_e32 v3, s4, v28
	v_lshlrev_b32_e32 v6, 11, v3
	v_bfe_u32 v3, v23, 16, 1
	v_lshl_add_u64 v[50:51], v[34:35], 0, v[6:7]
	v_add3_u32 v3, v23, v3, s9
	v_bfe_u32 v6, v37, 16, 1
	v_lshrrev_b32_e32 v3, 16, v3
	v_add3_u32 v6, v37, v6, s9
	global_store_dwordx4 v[50:51], v[30:33], off sc0 sc1
	s_nop 1
	v_and_or_b32 v30, v6, s10, v3
	v_bfe_u32 v3, v39, 16, 1
	v_add3_u32 v3, v39, v3, s9
	v_bfe_u32 v6, v41, 16, 1
	v_lshrrev_b32_e32 v3, 16, v3
	v_add3_u32 v6, v41, v6, s9
	v_and_or_b32 v31, v6, s10, v3
	v_bfe_u32 v3, v43, 16, 1
	v_add3_u32 v3, v43, v3, s9
	v_bfe_u32 v6, v45, 16, 1
	v_lshrrev_b32_e32 v3, 16, v3
	v_add3_u32 v6, v45, v6, s9
	v_and_or_b32 v32, v6, s10, v3
	v_bfe_u32 v3, v47, 16, 1
	v_add3_u32 v3, v47, v3, s9
	v_bfe_u32 v6, v49, 16, 1
	v_lshrrev_b32_e32 v3, 16, v3
	v_add3_u32 v6, v49, v6, s9
	v_and_or_b32 v33, v6, s10, v3
	v_or_b32_e32 v3, s4, v29
	v_lshlrev_b32_e32 v6, 11, v3
	v_lshl_add_u64 v[22:23], v[34:35], 0, v[6:7]
	global_store_dwordx4 v[22:23], v[30:33], off sc0 sc1
	s_waitcnt lgkmcnt(0)
	s_mov_b64 s[4:5], 0

; __device__ __forceinline__ void p0_transpose_item(const float* W, int K, int ldw, int c0, int nblk, bf16* WT, int row_off, const float* ks, LAS float* scr, int item, int lane) {
;     const int kb = item / nblk, nb = item % nblk, k0 = 64 * kb, n0 = 32 * nb;
; #pragma unroll 8
;     for (int i = 0; i < 32; ++i) { const int kk = 2 * i + (lane >> 5); float v = W[(size_t)(k0 + kk) * ldw + c0 + n0 + (lane & 31)]; if (ks) v *= ks[k0 + kk]; scr[kk * 33 + (lane & 31)] = v; }
.LBB0_36:
	s_lshl_b32 s14, s0, 1
	s_lshl_b32 s15, s6, 1
	v_or_b32_e32 v24, s14, v3
	v_or_b32_e32 v30, s15, v6
	s_add_i32 s16, s14, 4
	s_add_i32 s17, s15, 4
	s_add_i32 s18, s14, 8
	s_add_i32 s19, s15, 8
	s_add_i32 s22, s14, 12
	s_add_i32 s23, s15, 12
	s_add_i32 s27, s14, 16
	s_add_i32 s28, s15, 16
	s_add_i32 s29, s14, 20
	s_add_i32 s30, s15, 20
	s_add_i32 s31, s14, 24
	s_add_i32 s33, s15, 24
	s_add_i32 s34, s14, 28
	s_add_i32 s35, s15, 28
	v_mad_u64_u32 v[30:31], s[12:13], v30, s11, v[22:23]
	v_mad_u64_u32 v[32:33], s[12:13], v24, s11, v[22:23]
	v_or_b32_e32 v24, s16, v3
	v_or_b32_e32 v34, s17, v6
	v_or_b32_e32 v40, s18, v3
	v_or_b32_e32 v38, s19, v6
	v_or_b32_e32 v44, s22, v3
	v_or_b32_e32 v42, s23, v6
	v_or_b32_e32 v48, s27, v3
	v_or_b32_e32 v46, s28, v6
	v_or_b32_e32 v52, s29, v3
	v_or_b32_e32 v50, s30, v6
	v_or_b32_e32 v56, s31, v3
	v_or_b32_e32 v54, s33, v6
	v_or_b32_e32 v60, s34, v3
	v_or_b32_e32 v58, s35, v6
	v_mad_u64_u32 v[34:35], s[12:13], v34, s11, v[22:23]
	v_mad_u64_u32 v[36:37], s[12:13], v24, s11, v[22:23]
	v_mad_u64_u32 v[38:39], s[12:13], v38, s11, v[22:23]
	v_mad_u64_u32 v[40:41], s[12:13], v40, s11, v[22:23]
	v_mad_u64_u32 v[42:43], s[12:13], v42, s11, v[22:23]
	v_mad_u64_u32 v[44:45], s[12:13], v44, s11, v[22:23]
	v_mad_u64_u32 v[46:47], s[12:13], v46, s11, v[22:23]
	v_mad_u64_u32 v[48:49], s[12:13], v48, s11, v[22:23]
	v_mad_u64_u32 v[50:51], s[12:13], v50, s11, v[22:23]
	v_mad_u64_u32 v[52:53], s[12:13], v52, s11, v[22:23]
	v_mad_u64_u32 v[54:55], s[12:13], v54, s11, v[22:23]
	v_mad_u64_u32 v[56:57], s[12:13], v56, s11, v[22:23]
	v_mad_u64_u32 v[58:59], s[12:13], v58, s11, v[22:23]
	v_mad_u64_u32 v[60:61], s[12:13], v60, s11, v[22:23]
	global_load_dword v24, v[30:31], off
	global_load_dword v62, v[32:33], off
	global_load_dword v63, v[34:35], off
	global_load_dword v64, v[36:37], off
	global_load_dword v65, v[38:39], off
	global_load_dword v66, v[40:41], off
	global_load_dword v67, v[42:43], off
	global_load_dword v68, v[44:45], off
	global_load_dword v69, v[46:47], off
	global_load_dword v70, v[48:49], off
	global_load_dword v71, v[50:51], off
	global_load_dword v72, v[52:53], off
	global_load_dword v73, v[54:55], off
	global_load_dword v74, v[56:57], off
	global_load_dword v75, v[58:59], off
	global_load_dword v76, v[60:61], off
	v_or_b32_e32 v32, s14, v1
	v_or_b32_e32 v30, s15, v2
	s_add_i32 s6, s6, 16
	s_add_i32 s0, s0, 16
	s_add_i32 s7, s7, -16
	v_mad_u64_u32 v[30:31], s[12:13], v30, s8, v[4:5]
	v_mad_u64_u32 v[32:33], s[12:13], v32, s8, v[4:5]
	v_or_b32_e32 v31, s16, v1
	v_or_b32_e32 v33, s17, v2
	v_or_b32_e32 v40, s18, v1
	v_or_b32_e32 v38, s19, v2
	v_or_b32_e32 v44, s22, v1
	v_or_b32_e32 v42, s23, v2
	v_or_b32_e32 v48, s27, v1
	v_or_b32_e32 v46, s28, v2
	v_or_b32_e32 v52, s29, v1
	v_or_b32_e32 v50, s30, v2
	v_or_b32_e32 v56, s31, v1
	v_or_b32_e32 v54, s33, v2
	v_or_b32_e32 v60, s34, v1
	v_or_b32_e32 v58, s35, v2
	s_cmp_lg_u32 s7, 0
	v_mad_u64_u32 v[34:35], s[12:13], v33, s8, v[4:5]
	v_mad_u64_u32 v[36:37], s[12:13], v31, s8, v[4:5]
	v_mad_u64_u32 v[38:39], s[12:13], v38, s8, v[4:5]
	v_mad_u64_u32 v[40:41], s[12:13], v40, s8, v[4:5]
	v_mad_u64_u32 v[42:43], s[12:13], v42, s8, v[4:5]
	v_mad_u64_u32 v[44:45], s[12:13], v44, s8, v[4:5]
	v_mad_u64_u32 v[46:47], s[12:13], v46, s8, v[4:5]
	v_mad_u64_u32 v[48:49], s[12:13], v48, s8, v[4:5]
	v_mad_u64_u32 v[50:51], s[12:13], v50, s8, v[4:5]
	v_mad_u64_u32 v[52:53], s[12:13], v52, s8, v[4:5]
	v_mad_u64_u32 v[54:55], s[12:13], v54, s8, v[4:5]
	v_mad_u64_u32 v[56:57], s[12:13], v56, s8, v[4:5]
	v_mad_u64_u32 v[58:59], s[12:13], v58, s8, v[4:5]
	v_mad_u64_u32 v[60:61], s[12:13], v60, s8, v[4:5]
	s_waitcnt vmcnt(15)
	ds_write_b32 v30, v24
	s_waitcnt vmcnt(14)
	ds_write_b32 v32, v62
	s_waitcnt vmcnt(13)
	ds_write_b32 v34, v63
	s_waitcnt vmcnt(12)
	ds_write_b32 v36, v64
	s_waitcnt vmcnt(11)
	ds_write_b32 v38, v65
	s_waitcnt vmcnt(10)
	ds_write_b32 v40, v66
	s_waitcnt vmcnt(9)
	ds_write_b32 v42, v67
	s_waitcnt vmcnt(8)
	ds_write_b32 v44, v68
	s_waitcnt vmcnt(7)
	ds_write_b32 v46, v69
	s_waitcnt vmcnt(6)
	ds_write_b32 v48, v70
	s_waitcnt vmcnt(5)
	ds_write_b32 v50, v71
	s_waitcnt vmcnt(4)
	ds_write_b32 v52, v72
	s_waitcnt vmcnt(3)
	ds_write_b32 v54, v73
	s_waitcnt vmcnt(2)
	ds_write_b32 v56, v74
	s_waitcnt vmcnt(1)
	ds_write_b32 v58, v75
	s_waitcnt vmcnt(0)
	ds_write_b32 v60, v76
	s_cbranch_scc1 .LBB0_36
; #define GAS __attribute__((address_space(1)))
; #define LAS __attribute__((address_space(3)))
; #define LDS_WAIT() asm volatile("s_waitcnt lgkmcnt(0)" ::: "memory")
; __device__ __forceinline__ unsigned pk2(float lo, float hi) { return f2bf(lo) | (f2bf(hi) << 16); }
; __device__ __forceinline__ void p0_transpose_item(const float* W, int K, int ldw, int c0, int nblk, bf16* WT, int row_off, const float* ks, LAS float* scr, int item, int lane) {
;     ...
;     LDS_WAIT(); asm volatile("" ::: "memory");
;     const int c = lane & 7;
; #pragma unroll
;     for (int j = 0; j < 4; ++j) { const int n = (lane >> 3) + 8 * j; const LAS float* s = scr + (8 * c) * 33 + n;
;         v4u o; o.x = pk2(s[0 * 33], s[1 * 33]); o.y = pk2(s[2 * 33], s[3 * 33]); o.z = pk2(s[4 * 33], s[5 * 33]); o.w = pk2(s[6 * 33], s[7 * 33]);
;         *(GAS v4u*)(WT + (size_t)(row_off + n0 + n) * K + k0 + 8 * c) = o; }
;     LDS_WAIT(); asm volatile("" ::: "memory");
	s_waitcnt lgkmcnt(0)
	ds_read2_b32 v[22:23], v26 offset1:8
	ds_read2_b32 v[36:37], v26 offset0:33 offset1:41
	ds_read2_b32 v[38:39], v26 offset0:66 offset1:74
	ds_read2_b32 v[40:41], v26 offset0:99 offset1:107
	ds_read2_b32 v[42:43], v26 offset0:132 offset1:140
	s_waitcnt lgkmcnt(4)
	v_bfe_u32 v3, v22, 16, 1
	v_add3_u32 v3, v22, v3, s9
	s_waitcnt lgkmcnt(3)
	v_bfe_u32 v6, v36, 16, 1
	v_lshrrev_b32_e32 v3, 16, v3
	v_add3_u32 v6, v36, v6, s9
	ds_read2_b32 v[44:45], v26 offset0:165 offset1:173
	v_and_or_b32 v30, v6, s10, v3
	s_waitcnt lgkmcnt(3)
	v_bfe_u32 v3, v38, 16, 1
	v_add3_u32 v3, v38, v3, s9
	s_waitcnt lgkmcnt(2)
	v_bfe_u32 v6, v40, 16, 1
	ds_read2_b32 v[46:47], v26 offset0:198 offset1:206
	v_lshrrev_b32_e32 v3, 16, v3
	v_add3_u32 v6, v40, v6, s9
	ds_read2_b32 v[48:49], v26 offset0:231 offset1:239
	v_and_or_b32 v31, v6, s10, v3
	s_waitcnt lgkmcnt(3)
	v_bfe_u32 v3, v42, 16, 1
	v_add3_u32 v3, v42, v3, s9
	s_waitcnt lgkmcnt(2)
	v_bfe_u32 v6, v44, 16, 1
	v_lshrrev_b32_e32 v3, 16, v3
	v_add3_u32 v6, v44, v6, s9
	v_and_or_b32 v32, v6, s10, v3
	s_waitcnt lgkmcnt(1)
	v_bfe_u32 v3, v46, 16, 1
	v_add3_u32 v3, v46, v3, s9
	s_waitcnt lgkmcnt(0)
	v_bfe_u32 v6, v48, 16, 1
	s_or_b32 s5, s5, 0xa00
	v_lshrrev_b32_e32 v3, 16, v3
	v_add3_u32 v6, v48, v6, s9
	s_lshl_b32 s0, s4, 1
	v_and_or_b32 v33, v6, s10, v3
	v_or_b32_e32 v3, s5, v5
	v_lshl_add_u64 v[34:35], v[10:11], 0, s[0:1]
	v_lshlrev_b32_e32 v6, 11, v3
	v_bfe_u32 v3, v23, 16, 1
	v_lshl_add_u64 v[50:51], v[34:35], 0, v[6:7]
	v_add3_u32 v3, v23, v3, s9
	v_bfe_u32 v6, v37, 16, 1
	v_lshrrev_b32_e32 v3, 16, v3
	v_add3_u32 v6, v37, v6, s9
	global_store_dwordx4 v[50:51], v[30:33], off sc0 sc1
	ds_read2_b32 v[22:23], v26 offset0:16 offset1:24
	s_nop 0
	v_and_or_b32 v30, v6, s10, v3
	v_bfe_u32 v3, v39, 16, 1
	v_add3_u32 v3, v39, v3, s9
	v_bfe_u32 v6, v41, 16, 1
	v_lshrrev_b32_e32 v3, 16, v3
	v_add3_u32 v6, v41, v6, s9
	v_and_or_b32 v31, v6, s10, v3
	v_bfe_u32 v3, v43, 16, 1
	v_add3_u32 v3, v43, v3, s9
	v_bfe_u32 v6, v45, 16, 1
	v_lshrrev_b32_e32 v3, 16, v3
	v_add3_u32 v6, v45, v6, s9
	v_and_or_b32 v32, v6, s10, v3
	v_bfe_u32 v3, v47, 16, 1
	v_add3_u32 v3, v47, v3, s9
	v_bfe_u32 v6, v49, 16, 1
	v_lshrrev_b32_e32 v3, 16, v3
	v_add3_u32 v6, v49, v6, s9
	v_and_or_b32 v33, v6, s10, v3
	v_or_b32_e32 v3, s5, v27
	v_lshlrev_b32_e32 v6, 11, v3
	v_lshl_add_u64 v[36:37], v[34:35], 0, v[6:7]
	global_store_dwordx4 v[36:37], v[30:33], off sc0 sc1
	ds_read2_b32 v[36:37], v26 offset0:49 offset1:57
	ds_read2_b32 v[38:39], v26 offset0:82 offset1:90
	ds_read2_b32 v[40:41], v26 offset0:115 offset1:123
	s_waitcnt lgkmcnt(3)
	v_bfe_u32 v3, v22, 16, 1
	v_add3_u32 v3, v22, v3, s9
	s_waitcnt lgkmcnt(2)
	v_bfe_u32 v6, v36, 16, 1
	ds_read2_b32 v[42:43], v26 offset0:148 offset1:156
	v_lshrrev_b32_e32 v3, 16, v3
	v_add3_u32 v6, v36, v6, s9
	ds_read2_b32 v[44:45], v26 offset0:181 offset1:189
	v_and_or_b32 v30, v6, s10, v3
	s_waitcnt lgkmcnt(3)
	v_bfe_u32 v3, v38, 16, 1
	v_add3_u32 v3, v38, v3, s9
	s_waitcnt lgkmcnt(2)
	v_bfe_u32 v6, v40, 16, 1
	ds_read2_b32 v[46:47], v26 offset0:214 offset1:222
	v_lshrrev_b32_e32 v3, 16, v3
	v_add3_u32 v6, v40, v6, s9
	ds_read2_b32 v[48:49], v26 offset0:247 offset1:255
	v_and_or_b32 v31, v6, s10, v3
	s_waitcnt lgkmcnt(3)
	v_bfe_u32 v3, v42, 16, 1
	v_add3_u32 v3, v42, v3, s9
	s_waitcnt lgkmcnt(2)
	v_bfe_u32 v6, v44, 16, 1
	v_lshrrev_b32_e32 v3, 16, v3
	v_add3_u32 v6, v44, v6, s9
	v_and_or_b32 v32, v6, s10, v3
	s_waitcnt lgkmcnt(1)
	v_bfe_u32 v3, v46, 16, 1
	v_add3_u32 v3, v46, v3, s9
	s_waitcnt lgkmcnt(0)
	v_bfe_u32 v6, v48, 16, 1
	v_lshrrev_b32_e32 v3, 16, v3
	v_add3_u32 v6, v48, v6, s9
	v_and_or_b32 v33, v6, s10, v3
	v_or_b32_e32 v3, s5, v28
	v_lshlrev_b32_e32 v6, 11, v3
	v_bfe_u32 v3, v23, 16, 1
	v_lshl_add_u64 v[50:51], v[34:35], 0, v[6:7]
	v_add3_u32 v3, v23, v3, s9
	v_bfe_u32 v6, v37, 16, 1
	v_lshrrev_b32_e32 v3, 16, v3
	v_add3_u32 v6, v37, v6, s9
	global_store_dwordx4 v[50:51], v[30:33], off sc0 sc1
	s_nop 1
	v_and_or_b32 v30, v6, s10, v3
	v_bfe_u32 v3, v39, 16, 1
	v_add3_u32 v3, v39, v3, s9
	v_bfe_u32 v6, v41, 16, 1
	v_lshrrev_b32_e32 v3, 16, v3
	v_add3_u32 v6, v41, v6, s9
	v_and_or_b32 v31, v6, s10, v3
	v_bfe_u32 v3, v43, 16, 1
	v_add3_u32 v3, v43, v3, s9
	v_bfe_u32 v6, v45, 16, 1
	v_lshrrev_b32_e32 v3, 16, v3
	v_add3_u32 v6, v45, v6, s9
	v_and_or_b32 v32, v6, s10, v3
	v_bfe_u32 v3, v47, 16, 1
	v_add3_u32 v3, v47, v3, s9
	v_bfe_u32 v6, v49, 16, 1
	v_lshrrev_b32_e32 v3, 16, v3
	v_add3_u32 v6, v49, v6, s9
	v_and_or_b32 v33, v6, s10, v3
	v_or_b32_e32 v3, s5, v29
	v_lshlrev_b32_e32 v6, 11, v3
	v_lshl_add_u64 v[22:23], v[34:35], 0, v[6:7]
	global_store_dwordx4 v[22:23], v[30:33], off sc0 sc1
	s_waitcnt lgkmcnt(0)

; __device__ __forceinline__ void p0_transpose_item(const float* W, int K, int ldw, int c0, int nblk, bf16* WT, int row_off, const float* ks, LAS float* scr, int item, int lane) {
;     const int kb = item / nblk, nb = item % nblk, k0 = 64 * kb, n0 = 32 * nb;
; #pragma unroll 8
;     for (int i = 0; i < 32; ++i) { const int kk = 2 * i + (lane >> 5); float v = W[(size_t)(k0 + kk) * ldw + c0 + n0 + (lane & 31)]; if (ks) v *= ks[k0 + kk]; scr[kk * 33 + (lane & 31)] = v; }
.LBB0_41:
	s_lshl_b32 s14, s0, 1
	s_lshl_b32 s15, s6, 1
	v_or_b32_e32 v24, s14, v3
	v_or_b32_e32 v30, s15, v6
	s_add_i32 s16, s14, 4
	s_add_i32 s17, s15, 4
	s_add_i32 s18, s14, 8
	s_add_i32 s19, s15, 8
	s_add_i32 s22, s14, 12
	s_add_i32 s23, s15, 12
	s_add_i32 s27, s14, 16
	s_add_i32 s28, s15, 16
	s_add_i32 s29, s14, 20
	s_add_i32 s30, s15, 20
	s_add_i32 s31, s14, 24
	s_add_i32 s33, s15, 24
	s_add_i32 s34, s14, 28
	s_add_i32 s35, s15, 28
	v_mad_u64_u32 v[30:31], s[12:13], v30, s11, v[22:23]
	v_mad_u64_u32 v[32:33], s[12:13], v24, s11, v[22:23]
	v_or_b32_e32 v24, s16, v3
	v_or_b32_e32 v34, s17, v6
	v_or_b32_e32 v40, s18, v3
	v_or_b32_e32 v38, s19, v6
	v_or_b32_e32 v44, s22, v3
	v_or_b32_e32 v42, s23, v6
	v_or_b32_e32 v48, s27, v3
	v_or_b32_e32 v46, s28, v6
	v_or_b32_e32 v52, s29, v3
	v_or_b32_e32 v50, s30, v6
	v_or_b32_e32 v56, s31, v3
	v_or_b32_e32 v54, s33, v6
	v_or_b32_e32 v60, s34, v3
	v_or_b32_e32 v58, s35, v6
	v_mad_u64_u32 v[34:35], s[12:13], v34, s11, v[22:23]
	v_mad_u64_u32 v[36:37], s[12:13], v24, s11, v[22:23]
	v_mad_u64_u32 v[38:39], s[12:13], v38, s11, v[22:23]
	v_mad_u64_u32 v[40:41], s[12:13], v40, s11, v[22:23]
	v_mad_u64_u32 v[42:43], s[12:13], v42, s11, v[22:23]
	v_mad_u64_u32 v[44:45], s[12:13], v44, s11, v[22:23]
	v_mad_u64_u32 v[46:47], s[12:13], v46, s11, v[22:23]
	v_mad_u64_u32 v[48:49], s[12:13], v48, s11, v[22:23]
	v_mad_u64_u32 v[50:51], s[12:13], v50, s11, v[22:23]
	v_mad_u64_u32 v[52:53], s[12:13], v52, s11, v[22:23]
	v_mad_u64_u32 v[54:55], s[12:13], v54, s11, v[22:23]
	v_mad_u64_u32 v[56:57], s[12:13], v56, s11, v[22:23]
	v_mad_u64_u32 v[58:59], s[12:13], v58, s11, v[22:23]
	v_mad_u64_u32 v[60:61], s[12:13], v60, s11, v[22:23]
	global_load_dword v24, v[30:31], off
	global_load_dword v62, v[32:33], off
	global_load_dword v63, v[34:35], off
	global_load_dword v64, v[36:37], off
	global_load_dword v65, v[38:39], off
	global_load_dword v66, v[40:41], off
	global_load_dword v67, v[42:43], off
	global_load_dword v68, v[44:45], off
	global_load_dword v69, v[46:47], off
	global_load_dword v70, v[48:49], off
	global_load_dword v71, v[50:51], off
	global_load_dword v72, v[52:53], off
	global_load_dword v73, v[54:55], off
	global_load_dword v74, v[56:57], off
	global_load_dword v75, v[58:59], off
	global_load_dword v76, v[60:61], off
	v_or_b32_e32 v32, s14, v1
	v_or_b32_e32 v30, s15, v2
	s_add_i32 s6, s6, 16
	s_add_i32 s0, s0, 16
	s_add_i32 s7, s7, -16
	v_mad_u64_u32 v[30:31], s[12:13], v30, s8, v[4:5]
	v_mad_u64_u32 v[32:33], s[12:13], v32, s8, v[4:5]
	v_or_b32_e32 v31, s16, v1
	v_or_b32_e32 v33, s17, v2
	v_or_b32_e32 v40, s18, v1
	v_or_b32_e32 v38, s19, v2
	v_or_b32_e32 v44, s22, v1
	v_or_b32_e32 v42, s23, v2
	v_or_b32_e32 v48, s27, v1
	v_or_b32_e32 v46, s28, v2
	v_or_b32_e32 v52, s29, v1
	v_or_b32_e32 v50, s30, v2
	v_or_b32_e32 v56, s31, v1
	v_or_b32_e32 v54, s33, v2
	v_or_b32_e32 v60, s34, v1
	v_or_b32_e32 v58, s35, v2
	s_cmp_lg_u32 s7, 0
	v_mad_u64_u32 v[34:35], s[12:13], v33, s8, v[4:5]
	v_mad_u64_u32 v[36:37], s[12:13], v31, s8, v[4:5]
	v_mad_u64_u32 v[38:39], s[12:13], v38, s8, v[4:5]
	v_mad_u64_u32 v[40:41], s[12:13], v40, s8, v[4:5]
	v_mad_u64_u32 v[42:43], s[12:13], v42, s8, v[4:5]
	v_mad_u64_u32 v[44:45], s[12:13], v44, s8, v[4:5]
	v_mad_u64_u32 v[46:47], s[12:13], v46, s8, v[4:5]
	v_mad_u64_u32 v[48:49], s[12:13], v48, s8, v[4:5]
	v_mad_u64_u32 v[50:51], s[12:13], v50, s8, v[4:5]
	v_mad_u64_u32 v[52:53], s[12:13], v52, s8, v[4:5]
	v_mad_u64_u32 v[54:55], s[12:13], v54, s8, v[4:5]
	v_mad_u64_u32 v[56:57], s[12:13], v56, s8, v[4:5]
	v_mad_u64_u32 v[58:59], s[12:13], v58, s8, v[4:5]
	v_mad_u64_u32 v[60:61], s[12:13], v60, s8, v[4:5]
	s_waitcnt vmcnt(15)
	ds_write_b32 v30, v24
	s_waitcnt vmcnt(14)
	ds_write_b32 v32, v62
	s_waitcnt vmcnt(13)
	ds_write_b32 v34, v63
	s_waitcnt vmcnt(12)
	ds_write_b32 v36, v64
	s_waitcnt vmcnt(11)
	ds_write_b32 v38, v65
	s_waitcnt vmcnt(10)
	ds_write_b32 v40, v66
	s_waitcnt vmcnt(9)
	ds_write_b32 v42, v67
	s_waitcnt vmcnt(8)
	ds_write_b32 v44, v68
	s_waitcnt vmcnt(7)
	ds_write_b32 v46, v69
	s_waitcnt vmcnt(6)
	ds_write_b32 v48, v70
	s_waitcnt vmcnt(5)
	ds_write_b32 v50, v71
	s_waitcnt vmcnt(4)
	ds_write_b32 v52, v72
	s_waitcnt vmcnt(3)
	ds_write_b32 v54, v73
	s_waitcnt vmcnt(2)
	ds_write_b32 v56, v74
	s_waitcnt vmcnt(1)
	ds_write_b32 v58, v75
	s_waitcnt vmcnt(0)
	ds_write_b32 v60, v76
	s_cbranch_scc1 .LBB0_41
; #define GAS __attribute__((address_space(1)))
; #define LAS __attribute__((address_space(3)))
; #define LDS_WAIT() asm volatile("s_waitcnt lgkmcnt(0)" ::: "memory")
; __device__ __forceinline__ unsigned pk2(float lo, float hi) { return f2bf(lo) | (f2bf(hi) << 16); }
; __device__ __forceinline__ void p0_transpose_item(const float* W, int K, int ldw, int c0, int nblk, bf16* WT, int row_off, const float* ks, LAS float* scr, int item, int lane) {
;     ...
;     LDS_WAIT(); asm volatile("" ::: "memory");
;     const int c = lane & 7;
; #pragma unroll
;     for (int j = 0; j < 4; ++j) { const int n = (lane >> 3) + 8 * j; const LAS float* s = scr + (8 * c) * 33 + n;
;         v4u o; o.x = pk2(s[0 * 33], s[1 * 33]); o.y = pk2(s[2 * 33], s[3 * 33]); o.z = pk2(s[4 * 33], s[5 * 33]); o.w = pk2(s[6 * 33], s[7 * 33]);
;         *(GAS v4u*)(WT + (size_t)(row_off + n0 + n) * K + k0 + 8 * c) = o; }
;     LDS_WAIT(); asm volatile("" ::: "memory");
	s_waitcnt lgkmcnt(0)
	ds_read2_b32 v[22:23], v26 offset1:8
	ds_read2_b32 v[36:37], v26 offset0:33 offset1:41
	ds_read2_b32 v[38:39], v26 offset0:66 offset1:74
	ds_read2_b32 v[40:41], v26 offset0:99 offset1:107
	ds_read2_b32 v[42:43], v26 offset0:132 offset1:140
	s_waitcnt lgkmcnt(4)
	v_bfe_u32 v3, v22, 16, 1
	v_add3_u32 v3, v22, v3, s9
	s_waitcnt lgkmcnt(3)
	v_bfe_u32 v6, v36, 16, 1
	v_lshrrev_b32_e32 v3, 16, v3
	v_add3_u32 v6, v36, v6, s9
	ds_read2_b32 v[44:45], v26 offset0:165 offset1:173
	v_and_or_b32 v30, v6, s10, v3
	s_waitcnt lgkmcnt(3)
	v_bfe_u32 v3, v38, 16, 1
	v_add3_u32 v3, v38, v3, s9
	s_waitcnt lgkmcnt(2)
	v_bfe_u32 v6, v40, 16, 1
	ds_read2_b32 v[46:47], v26 offset0:198 offset1:206
	v_lshrrev_b32_e32 v3, 16, v3
	v_add3_u32 v6, v40, v6, s9
	ds_read2_b32 v[48:49], v26 offset0:231 offset1:239
	v_and_or_b32 v31, v6, s10, v3
	s_waitcnt lgkmcnt(3)
	v_bfe_u32 v3, v42, 16, 1
	v_add3_u32 v3, v42, v3, s9
	s_waitcnt lgkmcnt(2)
	v_bfe_u32 v6, v44, 16, 1
	v_lshrrev_b32_e32 v3, 16, v3
	v_add3_u32 v6, v44, v6, s9
	v_and_or_b32 v32, v6, s10, v3
	s_waitcnt lgkmcnt(1)
	v_bfe_u32 v3, v46, 16, 1
	v_add3_u32 v3, v46, v3, s9
	s_waitcnt lgkmcnt(0)
	v_bfe_u32 v6, v48, 16, 1
	s_bitset1_b32 s5, 11
	v_lshrrev_b32_e32 v3, 16, v3
	v_add3_u32 v6, v48, v6, s9
	s_lshl_b32 s0, s4, 1
	v_and_or_b32 v33, v6, s10, v3
	v_or_b32_e32 v3, s5, v5
	v_lshl_add_u64 v[34:35], v[10:11], 0, s[0:1]
	v_lshlrev_b32_e32 v6, 11, v3
	v_bfe_u32 v3, v23, 16, 1
	v_lshl_add_u64 v[50:51], v[34:35], 0, v[6:7]
	v_add3_u32 v3, v23, v3, s9
	v_bfe_u32 v6, v37, 16, 1
	v_lshrrev_b32_e32 v3, 16, v3
	v_add3_u32 v6, v37, v6, s9
	global_store_dwordx4 v[50:51], v[30:33], off sc0 sc1
	ds_read2_b32 v[22:23], v26 offset0:16 offset1:24
	s_nop 0
	v_and_or_b32 v30, v6, s10, v3
	v_bfe_u32 v3, v39, 16, 1
	v_add3_u32 v3, v39, v3, s9
	v_bfe_u32 v6, v41, 16, 1
	v_lshrrev_b32_e32 v3, 16, v3
	v_add3_u32 v6, v41, v6, s9
	v_and_or_b32 v31, v6, s10, v3
	v_bfe_u32 v3, v43, 16, 1
	v_add3_u32 v3, v43, v3, s9
	v_bfe_u32 v6, v45, 16, 1
	v_lshrrev_b32_e32 v3, 16, v3
	v_add3_u32 v6, v45, v6, s9
	v_and_or_b32 v32, v6, s10, v3
	v_bfe_u32 v3, v47, 16, 1
	v_add3_u32 v3, v47, v3, s9
	v_bfe_u32 v6, v49, 16, 1
	v_lshrrev_b32_e32 v3, 16, v3
	v_add3_u32 v6, v49, v6, s9
	v_and_or_b32 v33, v6, s10, v3
	v_or_b32_e32 v3, s5, v27
	v_lshlrev_b32_e32 v6, 11, v3
	v_lshl_add_u64 v[36:37], v[34:35], 0, v[6:7]
	global_store_dwordx4 v[36:37], v[30:33], off sc0 sc1
	ds_read2_b32 v[36:37], v26 offset0:49 offset1:57
	ds_read2_b32 v[38:39], v26 offset0:82 offset1:90
	ds_read2_b32 v[40:41], v26 offset0:115 offset1:123
	s_waitcnt lgkmcnt(3)
	v_bfe_u32 v3, v22, 16, 1
	v_add3_u32 v3, v22, v3, s9
	s_waitcnt lgkmcnt(2)
	v_bfe_u32 v6, v36, 16, 1
	ds_read2_b32 v[42:43], v26 offset0:148 offset1:156
	v_lshrrev_b32_e32 v3, 16, v3
	v_add3_u32 v6, v36, v6, s9
	ds_read2_b32 v[44:45], v26 offset0:181 offset1:189
	v_and_or_b32 v30, v6, s10, v3
	s_waitcnt lgkmcnt(3)
	v_bfe_u32 v3, v38, 16, 1
	v_add3_u32 v3, v38, v3, s9
	s_waitcnt lgkmcnt(2)
	v_bfe_u32 v6, v40, 16, 1
	ds_read2_b32 v[46:47], v26 offset0:214 offset1:222
	v_lshrrev_b32_e32 v3, 16, v3
	v_add3_u32 v6, v40, v6, s9
	ds_read2_b32 v[48:49], v26 offset0:247 offset1:255
	v_and_or_b32 v31, v6, s10, v3
	s_waitcnt lgkmcnt(3)
	v_bfe_u32 v3, v42, 16, 1
	v_add3_u32 v3, v42, v3, s9
	s_waitcnt lgkmcnt(2)
	v_bfe_u32 v6, v44, 16, 1
	v_lshrrev_b32_e32 v3, 16, v3
	v_add3_u32 v6, v44, v6, s9
	v_and_or_b32 v32, v6, s10, v3
	s_waitcnt lgkmcnt(1)
	v_bfe_u32 v3, v46, 16, 1
	v_add3_u32 v3, v46, v3, s9
	s_waitcnt lgkmcnt(0)
	v_bfe_u32 v6, v48, 16, 1
	v_lshrrev_b32_e32 v3, 16, v3
	v_add3_u32 v6, v48, v6, s9
	v_and_or_b32 v33, v6, s10, v3
	v_or_b32_e32 v3, s5, v28
	v_lshlrev_b32_e32 v6, 11, v3
	v_bfe_u32 v3, v23, 16, 1
	v_lshl_add_u64 v[50:51], v[34:35], 0, v[6:7]
	v_add3_u32 v3, v23, v3, s9
	v_bfe_u32 v6, v37, 16, 1
	v_lshrrev_b32_e32 v3, 16, v3
	v_add3_u32 v6, v37, v6, s9
	global_store_dwordx4 v[50:51], v[30:33], off sc0 sc1
	s_nop 1
	v_and_or_b32 v30, v6, s10, v3
	v_bfe_u32 v3, v39, 16, 1
	v_add3_u32 v3, v39, v3, s9
	v_bfe_u32 v6, v41, 16, 1
	v_lshrrev_b32_e32 v3, 16, v3
	v_add3_u32 v6, v41, v6, s9
	v_and_or_b32 v31, v6, s10, v3
	v_bfe_u32 v3, v43, 16, 1
	v_add3_u32 v3, v43, v3, s9
	v_bfe_u32 v6, v45, 16, 1
	v_lshrrev_b32_e32 v3, 16, v3
	v_add3_u32 v6, v45, v6, s9
	v_and_or_b32 v32, v6, s10, v3
	v_bfe_u32 v3, v47, 16, 1
	v_add3_u32 v3, v47, v3, s9
	v_bfe_u32 v6, v49, 16, 1
	v_lshrrev_b32_e32 v3, 16, v3
	v_add3_u32 v6, v49, v6, s9
	v_and_or_b32 v33, v6, s10, v3
	v_or_b32_e32 v3, s5, v29
	v_lshlrev_b32_e32 v6, 11, v3
	v_lshl_add_u64 v[22:23], v[34:35], 0, v[6:7]
	global_store_dwordx4 v[22:23], v[30:33], off sc0 sc1
	s_waitcnt lgkmcnt(0)

; __device__ __forceinline__ void p0_transpose_item(const float* W, int K, int ldw, int c0, int nblk, bf16* WT, int row_off, const float* ks, LAS float* scr, int item, int lane) {
;     const int kb = item / nblk, nb = item % nblk, k0 = 64 * kb, n0 = 32 * nb;
; #pragma unroll 8
;     for (int i = 0; i < 32; ++i) { const int kk = 2 * i + (lane >> 5); float v = W[(size_t)(k0 + kk) * ldw + c0 + n0 + (lane & 31)]; if (ks) v *= ks[k0 + kk]; scr[kk * 33 + (lane & 31)] = v; }
.LBB0_46:
	s_lshl_b32 s14, s0, 1
	s_lshl_b32 s15, s6, 1
	v_or_b32_e32 v24, s14, v3
	v_or_b32_e32 v30, s15, v6
	s_add_i32 s16, s14, 4
	s_add_i32 s17, s15, 4
	s_add_i32 s18, s14, 8
	s_add_i32 s19, s15, 8
	s_add_i32 s22, s14, 12
	s_add_i32 s23, s15, 12
	s_add_i32 s27, s14, 16
	s_add_i32 s28, s15, 16
	s_add_i32 s29, s14, 20
	s_add_i32 s30, s15, 20
	s_add_i32 s31, s14, 24
	s_add_i32 s33, s15, 24
	s_add_i32 s34, s14, 28
	s_add_i32 s35, s15, 28
	v_mad_u64_u32 v[30:31], s[12:13], v30, s11, v[22:23]
	v_mad_u64_u32 v[32:33], s[12:13], v24, s11, v[22:23]
	v_or_b32_e32 v24, s16, v3
	v_or_b32_e32 v34, s17, v6
	v_or_b32_e32 v40, s18, v3
	v_or_b32_e32 v38, s19, v6
	v_or_b32_e32 v44, s22, v3
	v_or_b32_e32 v42, s23, v6
	v_or_b32_e32 v48, s27, v3
	v_or_b32_e32 v46, s28, v6
	v_or_b32_e32 v52, s29, v3
	v_or_b32_e32 v50, s30, v6
	v_or_b32_e32 v56, s31, v3
	v_or_b32_e32 v54, s33, v6
	v_or_b32_e32 v60, s34, v3
	v_or_b32_e32 v58, s35, v6
	v_mad_u64_u32 v[34:35], s[12:13], v34, s11, v[22:23]
	v_mad_u64_u32 v[36:37], s[12:13], v24, s11, v[22:23]
	v_mad_u64_u32 v[38:39], s[12:13], v38, s11, v[22:23]
	v_mad_u64_u32 v[40:41], s[12:13], v40, s11, v[22:23]
	v_mad_u64_u32 v[42:43], s[12:13], v42, s11, v[22:23]
	v_mad_u64_u32 v[44:45], s[12:13], v44, s11, v[22:23]
	v_mad_u64_u32 v[46:47], s[12:13], v46, s11, v[22:23]
	v_mad_u64_u32 v[48:49], s[12:13], v48, s11, v[22:23]
	v_mad_u64_u32 v[50:51], s[12:13], v50, s11, v[22:23]
	v_mad_u64_u32 v[52:53], s[12:13], v52, s11, v[22:23]
	v_mad_u64_u32 v[54:55], s[12:13], v54, s11, v[22:23]
	v_mad_u64_u32 v[56:57], s[12:13], v56, s11, v[22:23]
	v_mad_u64_u32 v[58:59], s[12:13], v58, s11, v[22:23]
	v_mad_u64_u32 v[60:61], s[12:13], v60, s11, v[22:23]
	global_load_dword v24, v[30:31], off
	global_load_dword v62, v[32:33], off
	global_load_dword v63, v[34:35], off
	global_load_dword v64, v[36:37], off
	global_load_dword v65, v[38:39], off
	global_load_dword v66, v[40:41], off
	global_load_dword v67, v[42:43], off
	global_load_dword v68, v[44:45], off
	global_load_dword v69, v[46:47], off
	global_load_dword v70, v[48:49], off
	global_load_dword v71, v[50:51], off
	global_load_dword v72, v[52:53], off
	global_load_dword v73, v[54:55], off
	global_load_dword v74, v[56:57], off
	global_load_dword v75, v[58:59], off
	global_load_dword v76, v[60:61], off
	v_or_b32_e32 v32, s14, v1
	v_or_b32_e32 v30, s15, v2
	s_add_i32 s6, s6, 16
	s_add_i32 s0, s0, 16
	s_add_i32 s7, s7, -16
	v_mad_u64_u32 v[30:31], s[12:13], v30, s8, v[4:5]
	v_mad_u64_u32 v[32:33], s[12:13], v32, s8, v[4:5]
	v_or_b32_e32 v31, s16, v1
	v_or_b32_e32 v33, s17, v2
	v_or_b32_e32 v40, s18, v1
	v_or_b32_e32 v38, s19, v2
	v_or_b32_e32 v44, s22, v1
	v_or_b32_e32 v42, s23, v2
	v_or_b32_e32 v48, s27, v1
	v_or_b32_e32 v46, s28, v2
	v_or_b32_e32 v52, s29, v1
	v_or_b32_e32 v50, s30, v2
	v_or_b32_e32 v56, s31, v1
	v_or_b32_e32 v54, s33, v2
	v_or_b32_e32 v60, s34, v1
	v_or_b32_e32 v58, s35, v2
	s_cmp_lg_u32 s7, 0
	v_mad_u64_u32 v[34:35], s[12:13], v33, s8, v[4:5]
	v_mad_u64_u32 v[36:37], s[12:13], v31, s8, v[4:5]
	v_mad_u64_u32 v[38:39], s[12:13], v38, s8, v[4:5]
	v_mad_u64_u32 v[40:41], s[12:13], v40, s8, v[4:5]
	v_mad_u64_u32 v[42:43], s[12:13], v42, s8, v[4:5]
	v_mad_u64_u32 v[44:45], s[12:13], v44, s8, v[4:5]
	v_mad_u64_u32 v[46:47], s[12:13], v46, s8, v[4:5]
	v_mad_u64_u32 v[48:49], s[12:13], v48, s8, v[4:5]
	v_mad_u64_u32 v[50:51], s[12:13], v50, s8, v[4:5]
	v_mad_u64_u32 v[52:53], s[12:13], v52, s8, v[4:5]
	v_mad_u64_u32 v[54:55], s[12:13], v54, s8, v[4:5]
	v_mad_u64_u32 v[56:57], s[12:13], v56, s8, v[4:5]
	v_mad_u64_u32 v[58:59], s[12:13], v58, s8, v[4:5]
	v_mad_u64_u32 v[60:61], s[12:13], v60, s8, v[4:5]
	s_waitcnt vmcnt(15)
	ds_write_b32 v30, v24
	s_waitcnt vmcnt(14)
	ds_write_b32 v32, v62
	s_waitcnt vmcnt(13)
	ds_write_b32 v34, v63
	s_waitcnt vmcnt(12)
	ds_write_b32 v36, v64
	s_waitcnt vmcnt(11)
	ds_write_b32 v38, v65
	s_waitcnt vmcnt(10)
	ds_write_b32 v40, v66
	s_waitcnt vmcnt(9)
	ds_write_b32 v42, v67
	s_waitcnt vmcnt(8)
	ds_write_b32 v44, v68
	s_waitcnt vmcnt(7)
	ds_write_b32 v46, v69
	s_waitcnt vmcnt(6)
	ds_write_b32 v48, v70
	s_waitcnt vmcnt(5)
	ds_write_b32 v50, v71
	s_waitcnt vmcnt(4)
	ds_write_b32 v52, v72
	s_waitcnt vmcnt(3)
	ds_write_b32 v54, v73
	s_waitcnt vmcnt(2)
	ds_write_b32 v56, v74
	s_waitcnt vmcnt(1)
	ds_write_b32 v58, v75
	s_waitcnt vmcnt(0)
	ds_write_b32 v60, v76
	s_cbranch_scc1 .LBB0_46
; #define GAS __attribute__((address_space(1)))
; #define LAS __attribute__((address_space(3)))
; #define LDS_WAIT() asm volatile("s_waitcnt lgkmcnt(0)" ::: "memory")
; __device__ __forceinline__ unsigned pk2(float lo, float hi) { return f2bf(lo) | (f2bf(hi) << 16); }
; __device__ __forceinline__ void p0_transpose_item(const float* W, int K, int ldw, int c0, int nblk, bf16* WT, int row_off, const float* ks, LAS float* scr, int item, int lane) {
;     ...
;     LDS_WAIT(); asm volatile("" ::: "memory");
;     const int c = lane & 7;
; #pragma unroll
;     for (int j = 0; j < 4; ++j) { const int n = (lane >> 3) + 8 * j; const LAS float* s = scr + (8 * c) * 33 + n;
;         v4u o; o.x = pk2(s[0 * 33], s[1 * 33]); o.y = pk2(s[2 * 33], s[3 * 33]); o.z = pk2(s[4 * 33], s[5 * 33]); o.w = pk2(s[6 * 33], s[7 * 33]);
;         *(GAS v4u*)(WT + (size_t)(row_off + n0 + n) * K + k0 + 8 * c) = o; }
;     LDS_WAIT(); asm volatile("" ::: "memory");
	s_waitcnt lgkmcnt(0)
	ds_read2_b32 v[22:23], v26 offset1:8
	ds_read2_b32 v[36:37], v26 offset0:33 offset1:41
	ds_read2_b32 v[38:39], v26 offset0:66 offset1:74
	ds_read2_b32 v[40:41], v26 offset0:99 offset1:107
	ds_read2_b32 v[42:43], v26 offset0:132 offset1:140
	s_waitcnt lgkmcnt(4)
	v_bfe_u32 v3, v22, 16, 1
	v_add3_u32 v3, v22, v3, s9
	s_waitcnt lgkmcnt(3)
	v_bfe_u32 v6, v36, 16, 1
	v_lshrrev_b32_e32 v3, 16, v3
	v_add3_u32 v6, v36, v6, s9
	ds_read2_b32 v[44:45], v26 offset0:165 offset1:173
	v_and_or_b32 v30, v6, s10, v3
	s_waitcnt lgkmcnt(3)
	v_bfe_u32 v3, v38, 16, 1
	v_add3_u32 v3, v38, v3, s9
	s_waitcnt lgkmcnt(2)
	v_bfe_u32 v6, v40, 16, 1
	ds_read2_b32 v[46:47], v26 offset0:198 offset1:206
	v_lshrrev_b32_e32 v3, 16, v3
	v_add3_u32 v6, v40, v6, s9
	ds_read2_b32 v[48:49], v26 offset0:231 offset1:239
	v_and_or_b32 v31, v6, s10, v3
	s_waitcnt lgkmcnt(3)
	v_bfe_u32 v3, v42, 16, 1
	v_add3_u32 v3, v42, v3, s9
	s_waitcnt lgkmcnt(2)
	v_bfe_u32 v6, v44, 16, 1
	v_lshrrev_b32_e32 v3, 16, v3
	v_add3_u32 v6, v44, v6, s9
	v_and_or_b32 v32, v6, s10, v3
	s_waitcnt lgkmcnt(1)
	v_bfe_u32 v3, v46, 16, 1
	v_add3_u32 v3, v46, v3, s9
	s_waitcnt lgkmcnt(0)
	v_bfe_u32 v6, v48, 16, 1
	s_or_b32 s5, s5, 0x600
	v_lshrrev_b32_e32 v3, 16, v3
	v_add3_u32 v6, v48, v6, s9
	s_lshl_b32 s0, s4, 1
	v_and_or_b32 v33, v6, s10, v3
	v_or_b32_e32 v3, s5, v5
	v_lshl_add_u64 v[34:35], v[10:11], 0, s[0:1]
	v_lshlrev_b32_e32 v6, 11, v3
	v_bfe_u32 v3, v23, 16, 1
	v_lshl_add_u64 v[50:51], v[34:35], 0, v[6:7]
	v_add3_u32 v3, v23, v3, s9
	v_bfe_u32 v6, v37, 16, 1
	v_lshrrev_b32_e32 v3, 16, v3
	v_add3_u32 v6, v37, v6, s9
	global_store_dwordx4 v[50:51], v[30:33], off sc0 sc1
	ds_read2_b32 v[22:23], v26 offset0:16 offset1:24
	s_nop 0
	v_and_or_b32 v30, v6, s10, v3
	v_bfe_u32 v3, v39, 16, 1
	v_add3_u32 v3, v39, v3, s9
	v_bfe_u32 v6, v41, 16, 1
	v_lshrrev_b32_e32 v3, 16, v3
	v_add3_u32 v6, v41, v6, s9
	v_and_or_b32 v31, v6, s10, v3
	v_bfe_u32 v3, v43, 16, 1
	v_add3_u32 v3, v43, v3, s9
	v_bfe_u32 v6, v45, 16, 1
	v_lshrrev_b32_e32 v3, 16, v3
	v_add3_u32 v6, v45, v6, s9
	v_and_or_b32 v32, v6, s10, v3
	v_bfe_u32 v3, v47, 16, 1
	v_add3_u32 v3, v47, v3, s9
	v_bfe_u32 v6, v49, 16, 1
	v_lshrrev_b32_e32 v3, 16, v3
	v_add3_u32 v6, v49, v6, s9
	v_and_or_b32 v33, v6, s10, v3
	v_or_b32_e32 v3, s5, v27
	v_lshlrev_b32_e32 v6, 11, v3
	v_lshl_add_u64 v[36:37], v[34:35], 0, v[6:7]
	global_store_dwordx4 v[36:37], v[30:33], off sc0 sc1
	ds_read2_b32 v[36:37], v26 offset0:49 offset1:57
	ds_read2_b32 v[38:39], v26 offset0:82 offset1:90
	ds_read2_b32 v[40:41], v26 offset0:115 offset1:123
	s_waitcnt lgkmcnt(3)
	v_bfe_u32 v3, v22, 16, 1
	v_add3_u32 v3, v22, v3, s9
	s_waitcnt lgkmcnt(2)
	v_bfe_u32 v6, v36, 16, 1
	ds_read2_b32 v[42:43], v26 offset0:148 offset1:156
	v_lshrrev_b32_e32 v3, 16, v3
	v_add3_u32 v6, v36, v6, s9
	ds_read2_b32 v[44:45], v26 offset0:181 offset1:189
	v_and_or_b32 v30, v6, s10, v3
	s_waitcnt lgkmcnt(3)
	v_bfe_u32 v3, v38, 16, 1
	v_add3_u32 v3, v38, v3, s9
	s_waitcnt lgkmcnt(2)
	v_bfe_u32 v6, v40, 16, 1
	ds_read2_b32 v[46:47], v26 offset0:214 offset1:222
	v_lshrrev_b32_e32 v3, 16, v3
	v_add3_u32 v6, v40, v6, s9
	ds_read2_b32 v[48:49], v26 offset0:247 offset1:255
	v_and_or_b32 v31, v6, s10, v3
	s_waitcnt lgkmcnt(3)
	v_bfe_u32 v3, v42, 16, 1
	v_add3_u32 v3, v42, v3, s9
	s_waitcnt lgkmcnt(2)
	v_bfe_u32 v6, v44, 16, 1
	v_lshrrev_b32_e32 v3, 16, v3
	v_add3_u32 v6, v44, v6, s9
	v_and_or_b32 v32, v6, s10, v3
	s_waitcnt lgkmcnt(1)
	v_bfe_u32 v3, v46, 16, 1
	v_add3_u32 v3, v46, v3, s9
	s_waitcnt lgkmcnt(0)
	v_bfe_u32 v6, v48, 16, 1
	v_lshrrev_b32_e32 v3, 16, v3
	v_add3_u32 v6, v48, v6, s9
	v_and_or_b32 v33, v6, s10, v3
	v_or_b32_e32 v3, s5, v28
	v_lshlrev_b32_e32 v6, 11, v3
	v_bfe_u32 v3, v23, 16, 1
	v_lshl_add_u64 v[50:51], v[34:35], 0, v[6:7]
	v_add3_u32 v3, v23, v3, s9
	v_bfe_u32 v6, v37, 16, 1
	v_lshrrev_b32_e32 v3, 16, v3
	v_add3_u32 v6, v37, v6, s9
	global_store_dwordx4 v[50:51], v[30:33], off sc0 sc1
	s_nop 1
	v_and_or_b32 v30, v6, s10, v3
	v_bfe_u32 v3, v39, 16, 1
	v_add3_u32 v3, v39, v3, s9
	v_bfe_u32 v6, v41, 16, 1
	v_lshrrev_b32_e32 v3, 16, v3
	v_add3_u32 v6, v41, v6, s9
	v_and_or_b32 v31, v6, s10, v3
	v_bfe_u32 v3, v43, 16, 1
	v_add3_u32 v3, v43, v3, s9
	v_bfe_u32 v6, v45, 16, 1
	v_lshrrev_b32_e32 v3, 16, v3
	v_add3_u32 v6, v45, v6, s9
	v_and_or_b32 v32, v6, s10, v3
	v_bfe_u32 v3, v47, 16, 1
	v_add3_u32 v3, v47, v3, s9
	v_bfe_u32 v6, v49, 16, 1
	v_lshrrev_b32_e32 v3, 16, v3
	v_add3_u32 v6, v49, v6, s9
	v_and_or_b32 v33, v6, s10, v3
	v_or_b32_e32 v3, s5, v29
	v_lshlrev_b32_e32 v6, 11, v3
	v_lshl_add_u64 v[22:23], v[34:35], 0, v[6:7]
	global_store_dwordx4 v[22:23], v[30:33], off sc0 sc1
	s_waitcnt lgkmcnt(0)

; __device__ __forceinline__ void p0_transpose_item(const float* W, int K, int ldw, int c0, int nblk, bf16* WT, int row_off, const float* ks, LAS float* scr, int item, int lane) {
;     const int kb = item / nblk, nb = item % nblk, k0 = 64 * kb, n0 = 32 * nb;
; #pragma unroll 8
;     for (int i = 0; i < 32; ++i) { const int kk = 2 * i + (lane >> 5); float v = W[(size_t)(k0 + kk) * ldw + c0 + n0 + (lane & 31)]; if (ks) v *= ks[k0 + kk]; scr[kk * 33 + (lane & 31)] = v; }
.LBB0_50:
	s_lshl_b32 s14, s0, 1
	s_lshl_b32 s15, s5, 1
	v_or_b32_e32 v24, s14, v3
	v_or_b32_e32 v30, s15, v6
	s_add_i32 s16, s14, 4
	s_add_i32 s17, s15, 4
	s_add_i32 s18, s14, 8
	s_add_i32 s19, s15, 8
	s_add_i32 s22, s14, 12
	s_add_i32 s23, s15, 12
	s_add_i32 s27, s14, 16
	s_add_i32 s28, s15, 16
	s_add_i32 s29, s14, 20
	s_add_i32 s30, s15, 20
	s_add_i32 s31, s14, 24
	s_add_i32 s33, s15, 24
	s_add_i32 s34, s14, 28
	s_add_i32 s35, s15, 28
	v_mad_i64_i32 v[30:31], s[12:13], v30, s11, v[22:23]
	v_mad_i64_i32 v[32:33], s[12:13], v24, s11, v[22:23]
	v_or_b32_e32 v24, s16, v3
	v_or_b32_e32 v34, s17, v6
	v_or_b32_e32 v40, s18, v3
	v_or_b32_e32 v38, s19, v6
	v_or_b32_e32 v44, s22, v3
	v_or_b32_e32 v42, s23, v6
	v_or_b32_e32 v48, s27, v3
	v_or_b32_e32 v46, s28, v6
	v_or_b32_e32 v52, s29, v3
	v_or_b32_e32 v50, s30, v6
	v_or_b32_e32 v56, s31, v3
	v_or_b32_e32 v54, s33, v6
	v_or_b32_e32 v60, s34, v3
	v_or_b32_e32 v58, s35, v6
	v_mad_i64_i32 v[34:35], s[12:13], v34, s11, v[22:23]
	v_mad_i64_i32 v[36:37], s[12:13], v24, s11, v[22:23]
	v_mad_i64_i32 v[38:39], s[12:13], v38, s11, v[22:23]
	v_mad_i64_i32 v[40:41], s[12:13], v40, s11, v[22:23]
	v_mad_i64_i32 v[42:43], s[12:13], v42, s11, v[22:23]
	v_mad_i64_i32 v[44:45], s[12:13], v44, s11, v[22:23]
	v_mad_i64_i32 v[46:47], s[12:13], v46, s11, v[22:23]
	v_mad_i64_i32 v[48:49], s[12:13], v48, s11, v[22:23]
	v_mad_i64_i32 v[50:51], s[12:13], v50, s11, v[22:23]
	v_mad_i64_i32 v[52:53], s[12:13], v52, s11, v[22:23]
	v_mad_i64_i32 v[54:55], s[12:13], v54, s11, v[22:23]
	v_mad_i64_i32 v[56:57], s[12:13], v56, s11, v[22:23]
	v_mad_i64_i32 v[58:59], s[12:13], v58, s11, v[22:23]
	v_mad_i64_i32 v[60:61], s[12:13], v60, s11, v[22:23]
	global_load_dword v24, v[30:31], off
	global_load_dword v62, v[32:33], off
	global_load_dword v63, v[34:35], off
	global_load_dword v64, v[36:37], off
	global_load_dword v65, v[38:39], off
	global_load_dword v66, v[40:41], off
	global_load_dword v67, v[42:43], off
	global_load_dword v68, v[44:45], off
	global_load_dword v69, v[46:47], off
	global_load_dword v70, v[48:49], off
	global_load_dword v71, v[50:51], off
	global_load_dword v72, v[52:53], off
	global_load_dword v73, v[54:55], off
	global_load_dword v74, v[56:57], off
	global_load_dword v75, v[58:59], off
	global_load_dword v76, v[60:61], off
	v_or_b32_e32 v32, s14, v1
	v_or_b32_e32 v30, s15, v2
	s_add_i32 s5, s5, 16
	s_add_i32 s0, s0, 16
	s_add_i32 s7, s7, -16
	v_mad_u64_u32 v[30:31], s[12:13], v30, s8, v[4:5]
	v_mad_u64_u32 v[32:33], s[12:13], v32, s8, v[4:5]
	v_or_b32_e32 v31, s16, v1
	v_or_b32_e32 v33, s17, v2
	v_or_b32_e32 v40, s18, v1
	v_or_b32_e32 v38, s19, v2
	v_or_b32_e32 v44, s22, v1
	v_or_b32_e32 v42, s23, v2
	v_or_b32_e32 v48, s27, v1
	v_or_b32_e32 v46, s28, v2
	v_or_b32_e32 v52, s29, v1
	v_or_b32_e32 v50, s30, v2
	v_or_b32_e32 v56, s31, v1
	v_or_b32_e32 v54, s33, v2
	v_or_b32_e32 v60, s34, v1
	v_or_b32_e32 v58, s35, v2
	s_cmp_lg_u32 s7, 0
	v_mad_u64_u32 v[34:35], s[12:13], v33, s8, v[4:5]
	v_mad_u64_u32 v[36:37], s[12:13], v31, s8, v[4:5]
	v_mad_u64_u32 v[38:39], s[12:13], v38, s8, v[4:5]
	v_mad_u64_u32 v[40:41], s[12:13], v40, s8, v[4:5]
	v_mad_u64_u32 v[42:43], s[12:13], v42, s8, v[4:5]
	v_mad_u64_u32 v[44:45], s[12:13], v44, s8, v[4:5]
	v_mad_u64_u32 v[46:47], s[12:13], v46, s8, v[4:5]
	v_mad_u64_u32 v[48:49], s[12:13], v48, s8, v[4:5]
	v_mad_u64_u32 v[50:51], s[12:13], v50, s8, v[4:5]
	v_mad_u64_u32 v[52:53], s[12:13], v52, s8, v[4:5]
	v_mad_u64_u32 v[54:55], s[12:13], v54, s8, v[4:5]
	v_mad_u64_u32 v[56:57], s[12:13], v56, s8, v[4:5]
	v_mad_u64_u32 v[58:59], s[12:13], v58, s8, v[4:5]
	v_mad_u64_u32 v[60:61], s[12:13], v60, s8, v[4:5]
	s_waitcnt vmcnt(15)
	ds_write_b32 v30, v24
	s_waitcnt vmcnt(14)
	ds_write_b32 v32, v62
	s_waitcnt vmcnt(13)
	ds_write_b32 v34, v63
	s_waitcnt vmcnt(12)
	ds_write_b32 v36, v64
	s_waitcnt vmcnt(11)
	ds_write_b32 v38, v65
	s_waitcnt vmcnt(10)
	ds_write_b32 v40, v66
	s_waitcnt vmcnt(9)
	ds_write_b32 v42, v67
	s_waitcnt vmcnt(8)
	ds_write_b32 v44, v68
	s_waitcnt vmcnt(7)
	ds_write_b32 v46, v69
	s_waitcnt vmcnt(6)
	ds_write_b32 v48, v70
	s_waitcnt vmcnt(5)
	ds_write_b32 v50, v71
	s_waitcnt vmcnt(4)
	ds_write_b32 v52, v72
	s_waitcnt vmcnt(3)
	ds_write_b32 v54, v73
	s_waitcnt vmcnt(2)
	ds_write_b32 v56, v74
	s_waitcnt vmcnt(1)
	ds_write_b32 v58, v75
	s_waitcnt vmcnt(0)
	ds_write_b32 v60, v76
	s_cbranch_scc1 .LBB0_50
; #define GAS __attribute__((address_space(1)))
; #define LAS __attribute__((address_space(3)))
; #define LDS_WAIT() asm volatile("s_waitcnt lgkmcnt(0)" ::: "memory")
; __device__ __forceinline__ unsigned pk2(float lo, float hi) { return f2bf(lo) | (f2bf(hi) << 16); }
; __device__ __forceinline__ void p0_transpose_item(const float* W, int K, int ldw, int c0, int nblk, bf16* WT, int row_off, const float* ks, LAS float* scr, int item, int lane) {
;     ...
;     LDS_WAIT(); asm volatile("" ::: "memory");
;     const int c = lane & 7;
; #pragma unroll
;     for (int j = 0; j < 4; ++j) { const int n = (lane >> 3) + 8 * j; const LAS float* s = scr + (8 * c) * 33 + n;
;         v4u o; o.x = pk2(s[0 * 33], s[1 * 33]); o.y = pk2(s[2 * 33], s[3 * 33]); o.z = pk2(s[4 * 33], s[5 * 33]); o.w = pk2(s[6 * 33], s[7 * 33]);
;         *(GAS v4u*)(WT + (size_t)(row_off + n0 + n) * K + k0 + 8 * c) = o; }
;     LDS_WAIT(); asm volatile("" ::: "memory");
; __device__ __forceinline__ void p0_prologue(const Params& P, LAS unsigned char* lds, int tid, int lane, int wave, int vcu, int G) {
;     ...
;         for (int it = gw; it < NITEMS; it += NGW) {
;             int r = it;
;             if (r < I_IN1) { p0_transpose_item(P.w_in, 1024, 3080, 0, 48, (bf16*)(ws + WS_WIN), 0, nullptr, scr, r, lane); continue; } r -= I_IN1;
;             if (r < I_IN2) { p0_transpose_item(P.w_in, 1024, 3080, 2056, 16, (bf16*)(ws + WS_WIN), 1536, nullptr, scr, r, lane); continue; } r -= I_IN2;
;             if (r < I_IN2) { p0_transpose_item(P.w_in, 1024, 3080, 1536, 16, (bf16*)(ws + WS_WIN), 2048, nullptr, scr, r, lane); continue; } r -= I_IN2;
;             if (r < I_IN2) { p0_transpose_item(P.w_in, 1024, 3080, 2568, 16, (bf16*)(ws + WS_WIN), 2560, nullptr, scr, r, lane); continue; } r -= I_IN2;
;             p0_transpose_item(P.xattn_wkv, 1024, 2048, 0, 64, (bf16*)(ws + WS_WKV), 0, nullptr, scr, r, lane);
;         }
	s_waitcnt lgkmcnt(0)
	ds_read2_b32 v[22:23], v26 offset1:8
	ds_read2_b32 v[36:37], v26 offset0:33 offset1:41
	ds_read2_b32 v[38:39], v26 offset0:66 offset1:74
	ds_read2_b32 v[40:41], v26 offset0:99 offset1:107
	ds_read2_b32 v[42:43], v26 offset0:132 offset1:140
	ds_read2_b32 v[44:45], v26 offset0:165 offset1:173
	s_waitcnt lgkmcnt(5)
	v_bfe_u32 v3, v22, 16, 1
	v_add3_u32 v3, v22, v3, s9
	s_waitcnt lgkmcnt(4)
	v_bfe_u32 v6, v36, 16, 1
	v_lshrrev_b32_e32 v3, 16, v3
	v_add3_u32 v6, v36, v6, s9
	v_and_or_b32 v30, v6, s10, v3
	s_waitcnt lgkmcnt(3)
	v_bfe_u32 v3, v38, 16, 1
	v_add3_u32 v3, v38, v3, s9
	s_waitcnt lgkmcnt(2)
	v_bfe_u32 v6, v40, 16, 1
	ds_read2_b32 v[46:47], v26 offset0:198 offset1:206
	v_lshrrev_b32_e32 v3, 16, v3
	v_add3_u32 v6, v40, v6, s9
	ds_read2_b32 v[48:49], v26 offset0:231 offset1:239
	v_and_or_b32 v31, v6, s10, v3
	s_waitcnt lgkmcnt(3)
	v_bfe_u32 v3, v42, 16, 1
	v_add3_u32 v3, v42, v3, s9
	s_waitcnt lgkmcnt(2)
	v_bfe_u32 v6, v44, 16, 1
	v_lshrrev_b32_e32 v3, 16, v3
	v_add3_u32 v6, v44, v6, s9
	v_and_or_b32 v32, v6, s10, v3
	s_waitcnt lgkmcnt(1)
	v_bfe_u32 v3, v46, 16, 1
	v_add3_u32 v3, v46, v3, s9
	s_waitcnt lgkmcnt(0)
	v_bfe_u32 v6, v48, 16, 1
	v_lshrrev_b32_e32 v3, 16, v3
	v_add3_u32 v6, v48, v6, s9
	v_or_b32_e32 v50, s4, v5
	s_ashr_i32 s7, s6, 31
	v_and_or_b32 v33, v6, s10, v3
	v_ashrrev_i32_e32 v51, 31, v50
	v_bfe_u32 v3, v23, 16, 1
	v_lshl_add_u64 v[34:35], s[6:7], 1, v[10:11]
	v_lshlrev_b64 v[50:51], 11, v[50:51]
	v_add3_u32 v3, v23, v3, s9
	v_bfe_u32 v6, v37, 16, 1
	v_lshl_add_u64 v[50:51], v[34:35], 0, v[50:51]
	v_lshrrev_b32_e32 v3, 16, v3
	v_add3_u32 v6, v37, v6, s9
	global_store_dwordx4 v[50:51], v[30:33], off sc0 sc1
	v_or_b32_e32 v22, s4, v27
	v_ashrrev_i32_e32 v23, 31, v22
	v_and_or_b32 v30, v6, s10, v3
	v_bfe_u32 v3, v39, 16, 1
	v_add3_u32 v3, v39, v3, s9
	v_bfe_u32 v6, v41, 16, 1
	v_lshrrev_b32_e32 v3, 16, v3
	v_add3_u32 v6, v41, v6, s9
	v_and_or_b32 v31, v6, s10, v3
	v_bfe_u32 v3, v43, 16, 1
	v_add3_u32 v3, v43, v3, s9
	v_bfe_u32 v6, v45, 16, 1
	v_lshrrev_b32_e32 v3, 16, v3
	v_add3_u32 v6, v45, v6, s9
	v_and_or_b32 v32, v6, s10, v3
	v_bfe_u32 v3, v47, 16, 1
	v_add3_u32 v3, v47, v3, s9
	v_bfe_u32 v6, v49, 16, 1
	v_lshrrev_b32_e32 v3, 16, v3
	v_add3_u32 v6, v49, v6, s9
	v_lshlrev_b64 v[22:23], 11, v[22:23]
	v_and_or_b32 v33, v6, s10, v3
	ds_read2_b32 v[36:37], v26 offset0:16 offset1:24
	v_lshl_add_u64 v[22:23], v[34:35], 0, v[22:23]
	global_store_dwordx4 v[22:23], v[30:33], off sc0 sc1
	ds_read2_b32 v[22:23], v26 offset0:49 offset1:57
	ds_read2_b32 v[38:39], v26 offset0:82 offset1:90
	ds_read2_b32 v[40:41], v26 offset0:115 offset1:123
	s_waitcnt lgkmcnt(3)
	v_bfe_u32 v3, v36, 16, 1
	v_add3_u32 v3, v36, v3, s9
	s_waitcnt lgkmcnt(2)
	v_bfe_u32 v6, v22, 16, 1
	ds_read2_b32 v[42:43], v26 offset0:148 offset1:156
	v_lshrrev_b32_e32 v3, 16, v3
	v_add3_u32 v6, v22, v6, s9
	ds_read2_b32 v[44:45], v26 offset0:181 offset1:189
	v_and_or_b32 v30, v6, s10, v3
	s_waitcnt lgkmcnt(3)
	v_bfe_u32 v3, v38, 16, 1
	v_add3_u32 v3, v38, v3, s9
	s_waitcnt lgkmcnt(2)
	v_bfe_u32 v6, v40, 16, 1
	ds_read2_b32 v[46:47], v26 offset0:214 offset1:222
	v_lshrrev_b32_e32 v3, 16, v3
	v_add3_u32 v6, v40, v6, s9
	ds_read2_b32 v[48:49], v26 offset0:247 offset1:255
	v_and_or_b32 v31, v6, s10, v3
	s_waitcnt lgkmcnt(3)
	v_bfe_u32 v3, v42, 16, 1
	v_add3_u32 v3, v42, v3, s9
	s_waitcnt lgkmcnt(2)
	v_bfe_u32 v6, v44, 16, 1
	v_lshrrev_b32_e32 v3, 16, v3
	v_add3_u32 v6, v44, v6, s9
	v_and_or_b32 v32, v6, s10, v3
	s_waitcnt lgkmcnt(1)
	v_bfe_u32 v3, v46, 16, 1
	v_add3_u32 v3, v46, v3, s9
	s_waitcnt lgkmcnt(0)
	v_bfe_u32 v6, v48, 16, 1
	v_lshrrev_b32_e32 v3, 16, v3
	v_add3_u32 v6, v48, v6, s9
	v_or_b32_e32 v50, s4, v28
	v_and_or_b32 v33, v6, s10, v3
	v_ashrrev_i32_e32 v51, 31, v50
	v_bfe_u32 v3, v37, 16, 1
	v_lshlrev_b64 v[50:51], 11, v[50:51]
	v_add3_u32 v3, v37, v3, s9
	v_bfe_u32 v6, v23, 16, 1
	v_lshl_add_u64 v[50:51], v[34:35], 0, v[50:51]
	v_lshrrev_b32_e32 v3, 16, v3
	v_add3_u32 v6, v23, v6, s9
	global_store_dwordx4 v[50:51], v[30:33], off sc0 sc1
	v_or_b32_e32 v22, s4, v29
	v_ashrrev_i32_e32 v23, 31, v22
	v_and_or_b32 v30, v6, s10, v3
	v_bfe_u32 v3, v39, 16, 1
	v_add3_u32 v3, v39, v3, s9
	v_bfe_u32 v6, v41, 16, 1
	v_lshrrev_b32_e32 v3, 16, v3
	v_add3_u32 v6, v41, v6, s9
	v_and_or_b32 v31, v6, s10, v3
	v_bfe_u32 v3, v43, 16, 1
	v_add3_u32 v3, v43, v3, s9
	v_bfe_u32 v6, v45, 16, 1
	v_lshrrev_b32_e32 v3, 16, v3
	v_add3_u32 v6, v45, v6, s9
	v_and_or_b32 v32, v6, s10, v3
	v_bfe_u32 v3, v47, 16, 1
	v_add3_u32 v3, v47, v3, s9
	v_bfe_u32 v6, v49, 16, 1
	v_lshrrev_b32_e32 v3, 16, v3
	v_add3_u32 v6, v49, v6, s9
	v_lshlrev_b64 v[22:23], 11, v[22:23]
	v_and_or_b32 v33, v6, s10, v3
	v_lshl_add_u64 v[22:23], v[34:35], 0, v[22:23]
	global_store_dwordx4 v[22:23], v[30:33], off sc0 sc1
	s_waitcnt lgkmcnt(0)
	s_branch .LBB0_25

; __device__ __forceinline__ unsigned pk2(float lo, float hi) { return f2bf(lo) | (f2bf(hi) << 16); }
; __device__ __forceinline__ void p0_prologue(const Params& P, LAS unsigned char* lds, int tid, int lane, int wave, int vcu, int G) {
;     ...
;         bf16* WT = (bf16*)(ws + WS_LRUWT);
;         for (int it = vcu * NWAVES * 64 + tid; it < 8 * 2 * 64 * 8; it += G * NWAVES * 64) {
;             const int i8 = it & 7, j = (it >> 3) & 63, m = (it >> 9) & 1, g = it >> 10;
;             const float* src = (m ? P.lru_wx : P.lru_wa) + (size_t)(g * 64 + 8 * i8) * 64 + j;
;             v4u o; o.x = pk2(src[0], src[64]); o.y = pk2(src[128], src[192]); o.z = pk2(src[256], src[320]); o.w = pk2(src[384], src[448]);
;             *(v4u*)(WT + (size_t)it * 8) = o;
;         }
.LBB0_54:
	v_ashrrev_i32_e32 v11, 4, v2
	v_and_b32_e32 v12, 56, v1
	v_and_b32_e32 v6, 0x200, v2
	v_lshrrev_b32_e32 v15, 1, v2
	v_and_or_b32 v14, v11, s5, v12
	v_cmp_eq_u32_e32 vcc, 0, v6
	v_and_b32_e32 v6, 0xfc, v15
	v_ashrrev_i32_e32 v15, 31, v14
	v_cndmask_b32_e32 v13, v3, v8, vcc
	v_cndmask_b32_e32 v12, v9, v10, vcc
	v_lshlrev_b64 v[14:15], 8, v[14:15]
	v_lshl_add_u64 v[12:13], v[12:13], 0, v[14:15]
	v_lshl_add_u64 v[12:13], v[12:13], 0, v[6:7]
	global_load_dword v6, v[12:13], off
	global_load_dword v11, v[12:13], off offset:256
	global_load_dword v14, v[12:13], off offset:512
	global_load_dword v15, v[12:13], off offset:768
	global_load_dword v16, v[12:13], off offset:1024
	global_load_dword v17, v[12:13], off offset:1280
	global_load_dword v18, v[12:13], off offset:1536
	s_nop 0
	global_load_dword v12, v[12:13], off offset:1792
	v_add_u32_e32 v2, s4, v2
	v_cmp_lt_i32_e32 vcc, s12, v2
	v_add_u32_e32 v1, s3, v1
	s_or_b64 s[8:9], vcc, s[8:9]
	s_waitcnt vmcnt(7)
	v_bfe_u32 v13, v6, 16, 1
	s_waitcnt vmcnt(6)
	v_bfe_u32 v19, v11, 16, 1
	s_waitcnt vmcnt(5)
	v_bfe_u32 v20, v14, 16, 1
	s_waitcnt vmcnt(4)
	v_bfe_u32 v21, v15, 16, 1
	s_waitcnt vmcnt(3)
	v_bfe_u32 v22, v16, 16, 1
	s_waitcnt vmcnt(2)
	v_bfe_u32 v23, v17, 16, 1
	s_waitcnt vmcnt(1)
	v_bfe_u32 v24, v18, 16, 1
	s_waitcnt vmcnt(0)
	v_bfe_u32 v25, v12, 16, 1
	v_add3_u32 v6, v6, v13, s10
	v_add3_u32 v13, v14, v20, s10
	v_add3_u32 v14, v15, v21, s10
	v_add3_u32 v15, v16, v22, s10
	v_add3_u32 v16, v17, v23, s10
	v_add3_u32 v17, v18, v24, s10
	v_add3_u32 v11, v11, v19, s10
	v_add3_u32 v18, v12, v25, s10
	v_lshrrev_b32_e32 v6, 16, v6
	v_lshrrev_b32_e32 v13, 16, v13
	v_lshrrev_b32_e32 v15, 16, v15
	v_lshrrev_b32_e32 v17, 16, v17
	v_and_or_b32 v12, v11, s11, v6
	v_and_or_b32 v13, v14, s11, v13
	v_and_or_b32 v14, v16, s11, v15
	v_and_or_b32 v15, v18, s11, v17
	global_store_dwordx4 v[4:5], v[12:15], off sc0 sc1
	v_lshl_add_u64 v[4:5], v[4:5], 0, s[6:7]
	s_andn2_b64 exec, exec, s[8:9]
	s_cbranch_execnz .LBB0_54

; __device__ __forceinline__ unsigned pk2(float lo, float hi) { return f2bf(lo) | (f2bf(hi) << 16); }
; __device__ __forceinline__ float siluf_(float x) { return x * __builtin_amdgcn_rcpf(1.0f + __expf(-x)); }
; #define REPS(k) for (bool again_ = true; again_; again_ = (((REP_MASK >> (k)) & 1) ? rep_again(MISC, bar) : false))
; __device__ __forceinline__ void gdn_gate_norm(const Params& P, size_t wi, size_t nw) {
;     unsigned char* ws = P.ws;
;     bf16* Y = (bf16*)((unsigned char*)P.out + OUT_Y); const v4u* Z = (const v4u*)(ws + WS_Z); const float* SSQG = P.out;
;     for (size_t i = wi; i < (size_t)T * 64; i += nw) {
;         const size_t t = i >> 6; const int c0 = (int)(i & 63) * 8, h = c0 >> 7;
;         const f32x4 q0 = *(const f32x4*)(SSQG + t * 32 + h * 8);
;         const float rstd = rsqrtf(((q0.x + q0.y) + (q0.z + q0.w)) * (1.0f / 128.0f) + 1e-6f);
;         const v4u o = *(const v4u*)(Y + t * 1024 + c0), z = Z[i];
;         const f32x4 w0 = *(const f32x4*)(P.gdn_norm_w + (c0 & 127)), w1 = *(const f32x4*)(P.gdn_norm_w + (c0 & 127) + 4);
;         float y[8];
;         y[0] = bflo(o.x) * rstd * w0.x * siluf_(bflo(z.x)); y[1] = bfhi(o.x) * rstd * w0.y * siluf_(bfhi(z.x));
;         y[2] = bflo(o.y) * rstd * w0.z * siluf_(bflo(z.y)); y[3] = bfhi(o.y) * rstd * w0.w * siluf_(bfhi(z.y));
;         y[4] = bflo(o.z) * rstd * w1.x * siluf_(bflo(z.z)); y[5] = bfhi(o.z) * rstd * w1.y * siluf_(bfhi(z.z));
;         y[6] = bflo(o.w) * rstd * w1.z * siluf_(bflo(z.w)); y[7] = bfhi(o.w) * rstd * w1.w * siluf_(bfhi(z.w));
;         v4u r; r.x = pk2(y[0], y[1]); r.y = pk2(y[2], y[3]); r.z = pk2(y[4], y[5]); r.w = pk2(y[6], y[7]);
;         *(v4u*)(Y + t * 1024 + c0) = r;
;     }
; }
; __global__ void __launch_bounds__(NWAVES * 64, 2) hybrid_fwd(Params P) {
;     ...
;     if (IN(4)) REPS(4) {
;         gdn_gate_norm(P, (size_t)bx * (NWAVES * 64) + tid, (size_t)G * (NWAVES * 64));
.LBB0_2269:
	s_cmp_lt_i32 s74, 5
	s_cselect_b64 s[4:5], -1, 0
	s_and_b64 s[4:5], s[4:5], s[0:1]
	s_andn2_b64 vcc, exec, s[4:5]
	s_cbranch_vccnz .LBB0_2274
	s_ashr_i32 s3, s2, 31
	s_lshl_b64 s[0:1], s[2:3], 9
	v_or_b32_e32 v2, s0, v0
	v_mov_b32_e32 v3, s1
	s_mov_b64 s[0:1], 0x100000
	v_cmp_gt_u64_e32 vcc, s[0:1], v[2:3]
	s_and_saveexec_b64 s[0:1], vcc
	v_readlane_b32 s8, v254, 4
	v_readlane_b32 s22, v254, 18
	v_readlane_b32 s23, v254, 19
	v_readlane_b32 s9, v254, 5
	v_readlane_b32 s10, v254, 6
	v_readlane_b32 s11, v254, 7
	v_readlane_b32 s12, v254, 8
	v_readlane_b32 s13, v254, 9
	v_readlane_b32 s14, v254, 10
	v_readlane_b32 s15, v254, 11
	v_readlane_b32 s16, v254, 12
	v_readlane_b32 s17, v254, 13
	v_readlane_b32 s18, v254, 14
	v_readlane_b32 s19, v254, 15
	v_readlane_b32 s20, v254, 16
	v_readlane_b32 s21, v254, 17
	s_cbranch_execz .LBB0_2273
	s_ashr_i32 s27, s26, 31
	s_lshl_b64 s[6:7], s[26:27], 9
	s_add_u32 s8, s94, 0x400000
	s_addc_u32 s9, s95, 0
	s_lshl_b64 s[10:11], s[2:3], 13
	s_add_u32 s10, s24, s10
	v_mov_b32_e32 v5, 0
	v_lshlrev_b32_e32 v4, 4, v0
	s_addc_u32 s11, s25, s11
	v_lshl_add_u64 v[6:7], s[10:11], 0, v[4:5]
	s_mov_b64 s[10:11], 0x7c00000
	v_lshlrev_b32_e32 v1, 3, v0
	v_lshl_add_u64 v[6:7], v[6:7], 0, s[10:11]
	s_lshl_b64 s[10:11], s[26:27], 13
	v_lshl_or_b32 v1, s2, 12, v1
	s_lshl_b32 s3, s26, 12
	s_mov_b64 s[12:13], 0
	v_mov_b32_e32 v8, 0x358637bd
	s_mov_b32 s16, 0x800000
	s_mov_b32 s17, 0xffff0000
	s_movk_i32 s18, 0x7fff
	s_mov_b64 s[14:15], 0xfffff
	v_mov_b32_e32 v87, 0
	v_lshrrev_b64 v[14:15], 6, v[2:3]
	global_load_dwordx4 v[10:13], v[6:7], off
	v_lshlrev_b32_e32 v4, 1, v2
	v_lshlrev_b64 v[22:23], 7, v[14:15]
	v_and_b32_e32 v16, 0x78, v1
	v_and_b32_e32 v4, 0x60, v4
	v_lshl_add_u64 v[22:23], s[94:95], 0, v[22:23]
	v_lshlrev_b64 v[24:25], 11, v[14:15]
	v_lshlrev_b32_e32 v26, 2, v16
	v_lshl_add_u64 v[22:23], v[22:23], 0, v[4:5]
	global_load_dwordx4 v[14:17], v26, s[22:23]
	global_load_dwordx4 v[18:21], v26, s[22:23] offset:16
	v_lshl_add_u64 v[26:27], s[8:9], 0, v[24:25]
	global_load_dwordx4 v[22:25], v[22:23], off
	v_and_b32_e32 v9, 0x1f8, v1
	v_lshlrev_b32_e32 v4, 1, v9
	v_lshl_add_u64 v[30:31], v[26:27], 0, v[4:5]
	global_load_dwordx4 v[26:29], v[30:31], off
	v_lshl_add_u64 v[2:3], v[2:3], 0, s[6:7]
	v_cmp_lt_u64_e32 vcc, s[14:15], v[2:3]
	s_or_b64 s[12:13], vcc, s[12:13]
	v_lshl_add_u64 v[6:7], v[6:7], 0, s[10:11]
	v_add_u32_e32 v1, s3, v1
	s_mov_b64 s[98:99], exec
	s_andn2_b64 exec, exec, s[12:13]
	s_cbranch_execz .Lp4_lastA
	v_lshrrev_b64 v[54:55], 6, v[2:3]
	global_load_dwordx4 v[50:53], v[6:7], off
	v_lshlrev_b32_e32 v86, 1, v2
	v_lshlrev_b64 v[62:63], 7, v[54:55]
	v_and_b32_e32 v56, 0x78, v1
	v_and_b32_e32 v86, 0x60, v86
	v_lshl_add_u64 v[62:63], s[94:95], 0, v[62:63]
	v_lshlrev_b64 v[64:65], 11, v[54:55]
	v_lshlrev_b32_e32 v66, 2, v56
	v_lshl_add_u64 v[62:63], v[62:63], 0, v[86:87]
	global_load_dwordx4 v[54:57], v66, s[22:23]
	global_load_dwordx4 v[58:61], v66, s[22:23] offset:16
	v_lshl_add_u64 v[66:67], s[8:9], 0, v[64:65]
	global_load_dwordx4 v[62:65], v[62:63], off
	v_and_b32_e32 v88, 0x1f8, v1
	v_lshlrev_b32_e32 v86, 1, v88
	v_lshl_add_u64 v[70:71], v[66:67], 0, v[86:87]
	global_load_dwordx4 v[66:69], v[70:71], off
	v_lshl_add_u64 v[2:3], v[2:3], 0, s[6:7]
	v_cmp_lt_u64_e32 vcc, s[14:15], v[2:3]
	s_or_b64 s[12:13], vcc, s[12:13]
	v_lshl_add_u64 v[6:7], v[6:7], 0, s[10:11]
	v_add_u32_e32 v1, s3, v1
	s_mov_b64 s[100:101], exec
	s_mov_b64 exec, s[98:99]
	s_waitcnt vmcnt(5)
	v_lshlrev_b32_e32 v32, 16, v10
	v_mul_f32_e32 v4, 0xbfb8aa3b, v32
	v_exp_f32_e32 v4, v4
	v_lshlrev_b32_e32 v33, 16, v11
	v_lshlrev_b32_e32 v35, 16, v13
	v_lshlrev_b32_e32 v34, 16, v12
	v_and_b32_e32 v13, 0xffff0000, v13
	v_and_b32_e32 v12, 0xffff0000, v12
	v_mov_b32_e32 v36, v14
	v_mov_b32_e32 v37, v16
	v_mov_b32_e32 v16, v15
	v_mov_b32_e32 v14, v18
	v_mov_b32_e32 v15, v20
	v_mov_b32_e32 v20, v19
	v_mov_b32_e32 v18, v23
	v_mov_b32_e32 v19, v24
	v_mov_b32_e32 v23, v25
	v_pk_add_f32 v[18:19], v[18:19], v[22:23]
	v_and_b32_e32 v11, 0xffff0000, v11
	v_add_f32_e32 v18, v18, v19
	v_and_b32_e32 v10, 0xffff0000, v10
	v_mul_f32_e32 v38, 0xbfb8aa3b, v33
	v_mul_f32_e32 v40, 0xbfb8aa3b, v34
	v_mul_f32_e32 v41, 0xbfb8aa3b, v12
	v_mul_f32_e32 v42, 0xbfb8aa3b, v35
	v_mul_f32_e32 v43, 0xbfb8aa3b, v13
	v_add_f32_e32 v4, 1.0, v4
	v_fmamk_f32 v45, v18, 0x3c000000, v8
	v_mul_f32_e32 v9, 0xbfb8aa3b, v10
	v_mul_f32_e32 v39, 0xbfb8aa3b, v11
	v_exp_f32_e32 v38, v38
	v_exp_f32_e32 v40, v40
	v_exp_f32_e32 v41, v41
	v_exp_f32_e32 v42, v42
	v_exp_f32_e32 v43, v43
	v_rcp_f32_e32 v18, v4
	v_mul_f32_e32 v4, 0x4b800000, v45
	v_cmp_gt_f32_e32 vcc, s16, v45
	v_exp_f32_e32 v9, v9
	v_exp_f32_e32 v39, v39
	v_cndmask_b32_e32 v4, v45, v4, vcc
	v_rsq_f32_e32 v4, v4
	v_add_f32_e32 v19, 1.0, v38
	v_add_f32_e32 v40, 1.0, v40
	v_add_f32_e32 v41, 1.0, v41
	v_add_f32_e32 v44, 1.0, v42
	v_add_f32_e32 v43, 1.0, v43
	v_add_f32_e32 v9, 1.0, v9
	v_add_f32_e32 v39, 1.0, v39
	v_rcp_f32_e32 v19, v19
	v_rcp_f32_e32 v40, v40
	v_rcp_f32_e32 v42, v41
	v_rcp_f32_e32 v41, v44
	v_rcp_f32_e32 v43, v43
	v_rcp_f32_e32 v38, v9
	v_rcp_f32_e32 v39, v39
	v_mul_f32_e32 v9, 0x45800000, v4
	v_lshlrev_b32_e32 v23, 16, v27
	v_lshlrev_b32_e32 v22, 16, v26
	v_and_b32_e32 v25, 0xffff0000, v27
	v_and_b32_e32 v24, 0xffff0000, v26
	v_lshlrev_b32_e32 v27, 16, v29
	v_lshlrev_b32_e32 v26, 16, v28
	v_and_b32_e32 v29, 0xffff0000, v29
	v_and_b32_e32 v28, 0xffff0000, v28
	v_cndmask_b32_e32 v4, v4, v9, vcc
	v_pk_mul_f32 v[22:23], v[4:5], v[22:23] op_sel_hi:[0,1]
	v_pk_mul_f32 v[26:27], v[4:5], v[26:27] op_sel_hi:[0,1]
	v_pk_mul_f32 v[28:29], v[4:5], v[28:29] op_sel_hi:[0,1]
	v_pk_mul_f32 v[18:19], v[18:19], v[32:33]
	v_pk_mul_f32 v[32:33], v[40:41], v[34:35]
	v_pk_mul_f32 v[12:13], v[42:43], v[12:13]
	v_pk_mul_f32 v[24:25], v[4:5], v[24:25] op_sel_hi:[0,1]
	v_pk_mul_f32 v[22:23], v[36:37], v[22:23]
	v_pk_mul_f32 v[14:15], v[14:15], v[26:27]
	v_pk_mul_f32 v[20:21], v[20:21], v[28:29]
	v_pk_mul_f32 v[10:11], v[38:39], v[10:11]
	v_pk_mul_f32 v[16:17], v[16:17], v[24:25]
	v_pk_mul_f32 v[18:19], v[18:19], v[22:23]
	v_pk_mul_f32 v[14:15], v[32:33], v[14:15]
	v_pk_mul_f32 v[12:13], v[12:13], v[20:21]
	v_pk_mul_f32 v[10:11], v[10:11], v[16:17]
	v_cvt_pk_bf16_f32 v10, v18, v10
	v_cvt_pk_bf16_f32 v11, v19, v11
	v_cvt_pk_bf16_f32 v12, v14, v12
	v_cvt_pk_bf16_f32 v13, v15, v13
	global_store_dwordx4 v[30:31], v[10:13], off sc0 sc1
	s_mov_b64 exec, s[100:101]
; __device__ __forceinline__ unsigned pk2(float lo, float hi) { return f2bf(lo) | (f2bf(hi) << 16); }
; __device__ __forceinline__ float siluf_(float x) { return x * __builtin_amdgcn_rcpf(1.0f + __expf(-x)); }
; __device__ __forceinline__ void gdn_gate_norm(const Params& P, size_t wi, size_t nw) {
;     ...
;     for (size_t i = wi; i < (size_t)T * 64; i += nw) {
;         const size_t t = i >> 6; const int c0 = (int)(i & 63) * 8, h = c0 >> 7;
;         const f32x4 q0 = *(const f32x4*)(SSQG + t * 32 + h * 8);
;         const float rstd = rsqrtf(((q0.x + q0.y) + (q0.z + q0.w)) * (1.0f / 128.0f) + 1e-6f);
;         const v4u o = *(const v4u*)(Y + t * 1024 + c0), z = Z[i];
;         const f32x4 w0 = *(const f32x4*)(P.gdn_norm_w + (c0 & 127)), w1 = *(const f32x4*)(P.gdn_norm_w + (c0 & 127) + 4);
;         float y[8];
;         y[0] = bflo(o.x) * rstd * w0.x * siluf_(bflo(z.x)); y[1] = bfhi(o.x) * rstd * w0.y * siluf_(bfhi(z.x));
;         y[2] = bflo(o.y) * rstd * w0.z * siluf_(bflo(z.y)); y[3] = bfhi(o.y) * rstd * w0.w * siluf_(bfhi(z.y));
;         y[4] = bflo(o.z) * rstd * w1.x * siluf_(bflo(z.z)); y[5] = bfhi(o.z) * rstd * w1.y * siluf_(bfhi(z.z));
;         y[6] = bflo(o.w) * rstd * w1.z * siluf_(bflo(z.w)); y[7] = bfhi(o.w) * rstd * w1.w * siluf_(bfhi(z.w));
;         v4u r; r.x = pk2(y[0], y[1]); r.y = pk2(y[2], y[3]); r.z = pk2(y[4], y[5]); r.w = pk2(y[6], y[7]);
;         *(v4u*)(Y + t * 1024 + c0) = r;
;     }
.Lp4_loop:
	s_mov_b64 s[98:99], exec
	s_andn2_b64 exec, exec, s[12:13]
	s_cbranch_execz .Lp4_lastB
	v_lshrrev_b64 v[14:15], 6, v[2:3]
	global_load_dwordx4 v[10:13], v[6:7], off
	v_lshlrev_b32_e32 v4, 1, v2
	v_lshlrev_b64 v[22:23], 7, v[14:15]
	v_and_b32_e32 v16, 0x78, v1
	v_and_b32_e32 v4, 0x60, v4
	v_lshl_add_u64 v[22:23], s[94:95], 0, v[22:23]
	v_lshlrev_b64 v[24:25], 11, v[14:15]
	v_lshlrev_b32_e32 v26, 2, v16
	v_lshl_add_u64 v[22:23], v[22:23], 0, v[4:5]
	global_load_dwordx4 v[14:17], v26, s[22:23]
	global_load_dwordx4 v[18:21], v26, s[22:23] offset:16
	v_lshl_add_u64 v[26:27], s[8:9], 0, v[24:25]
	global_load_dwordx4 v[22:25], v[22:23], off
	v_and_b32_e32 v9, 0x1f8, v1
	v_lshlrev_b32_e32 v4, 1, v9
	v_lshl_add_u64 v[30:31], v[26:27], 0, v[4:5]
	global_load_dwordx4 v[26:29], v[30:31], off
	v_lshl_add_u64 v[2:3], v[2:3], 0, s[6:7]
	v_cmp_lt_u64_e32 vcc, s[14:15], v[2:3]
	s_or_b64 s[12:13], vcc, s[12:13]
	v_lshl_add_u64 v[6:7], v[6:7], 0, s[10:11]
	v_add_u32_e32 v1, s3, v1
	s_mov_b64 s[100:101], exec
	s_mov_b64 exec, s[98:99]
	s_waitcnt vmcnt(6)
	v_lshlrev_b32_e32 v72, 16, v50
	v_mul_f32_e32 v86, 0xbfb8aa3b, v72
	v_exp_f32_e32 v86, v86
	v_lshlrev_b32_e32 v73, 16, v51
	v_lshlrev_b32_e32 v75, 16, v53
	v_lshlrev_b32_e32 v74, 16, v52
	v_and_b32_e32 v53, 0xffff0000, v53
	v_and_b32_e32 v52, 0xffff0000, v52
	v_mov_b32_e32 v76, v54
	v_mov_b32_e32 v77, v56
	v_mov_b32_e32 v56, v55
	v_mov_b32_e32 v54, v58
	v_mov_b32_e32 v55, v60
	v_mov_b32_e32 v60, v59
	v_mov_b32_e32 v58, v63
	v_mov_b32_e32 v59, v64
	v_mov_b32_e32 v63, v65
	v_pk_add_f32 v[58:59], v[58:59], v[62:63]
	v_and_b32_e32 v51, 0xffff0000, v51
	v_add_f32_e32 v58, v58, v59
	v_and_b32_e32 v50, 0xffff0000, v50
	v_mul_f32_e32 v78, 0xbfb8aa3b, v73
	v_mul_f32_e32 v80, 0xbfb8aa3b, v74
	v_mul_f32_e32 v81, 0xbfb8aa3b, v52
	v_mul_f32_e32 v82, 0xbfb8aa3b, v75
	v_mul_f32_e32 v83, 0xbfb8aa3b, v53
	v_add_f32_e32 v86, 1.0, v86
	v_fmamk_f32 v85, v58, 0x3c000000, v8
	v_mul_f32_e32 v88, 0xbfb8aa3b, v50
	v_mul_f32_e32 v79, 0xbfb8aa3b, v51
	v_exp_f32_e32 v78, v78
	v_exp_f32_e32 v80, v80
	v_exp_f32_e32 v81, v81
	v_exp_f32_e32 v82, v82
	v_exp_f32_e32 v83, v83
	v_rcp_f32_e32 v58, v86
	v_mul_f32_e32 v86, 0x4b800000, v85
	v_cmp_gt_f32_e32 vcc, s16, v85
	v_exp_f32_e32 v88, v88
	v_exp_f32_e32 v79, v79
	v_cndmask_b32_e32 v86, v85, v86, vcc
	v_rsq_f32_e32 v86, v86
	v_add_f32_e32 v59, 1.0, v78
	v_add_f32_e32 v80, 1.0, v80
	v_add_f32_e32 v81, 1.0, v81
	v_add_f32_e32 v84, 1.0, v82
	v_add_f32_e32 v83, 1.0, v83
	v_add_f32_e32 v88, 1.0, v88
	v_add_f32_e32 v79, 1.0, v79
	v_rcp_f32_e32 v59, v59
	v_rcp_f32_e32 v80, v80
	v_rcp_f32_e32 v82, v81
	v_rcp_f32_e32 v81, v84
	v_rcp_f32_e32 v83, v83
	v_rcp_f32_e32 v78, v88
	v_rcp_f32_e32 v79, v79
	v_mul_f32_e32 v88, 0x45800000, v86
	v_lshlrev_b32_e32 v63, 16, v67
	v_lshlrev_b32_e32 v62, 16, v66
	v_and_b32_e32 v65, 0xffff0000, v67
	v_and_b32_e32 v64, 0xffff0000, v66
	v_lshlrev_b32_e32 v67, 16, v69
	v_lshlrev_b32_e32 v66, 16, v68
	v_and_b32_e32 v69, 0xffff0000, v69
	v_and_b32_e32 v68, 0xffff0000, v68
	v_cndmask_b32_e32 v86, v86, v88, vcc
	v_pk_mul_f32 v[62:63], v[86:87], v[62:63] op_sel_hi:[0,1]
	v_pk_mul_f32 v[66:67], v[86:87], v[66:67] op_sel_hi:[0,1]
	v_pk_mul_f32 v[68:69], v[86:87], v[68:69] op_sel_hi:[0,1]
	v_pk_mul_f32 v[58:59], v[58:59], v[72:73]
	v_pk_mul_f32 v[72:73], v[80:81], v[74:75]
	v_pk_mul_f32 v[52:53], v[82:83], v[52:53]
	v_pk_mul_f32 v[64:65], v[86:87], v[64:65] op_sel_hi:[0,1]
	v_pk_mul_f32 v[62:63], v[76:77], v[62:63]
	v_pk_mul_f32 v[54:55], v[54:55], v[66:67]
	v_pk_mul_f32 v[60:61], v[60:61], v[68:69]
	v_pk_mul_f32 v[50:51], v[78:79], v[50:51]
	v_pk_mul_f32 v[56:57], v[56:57], v[64:65]
	v_pk_mul_f32 v[58:59], v[58:59], v[62:63]
	v_pk_mul_f32 v[54:55], v[72:73], v[54:55]
	v_pk_mul_f32 v[52:53], v[52:53], v[60:61]
	v_pk_mul_f32 v[50:51], v[50:51], v[56:57]
	v_cvt_pk_bf16_f32 v50, v58, v50
	v_cvt_pk_bf16_f32 v51, v59, v51
	v_cvt_pk_bf16_f32 v52, v54, v52
	v_cvt_pk_bf16_f32 v53, v55, v53
	global_store_dwordx4 v[70:71], v[50:53], off sc0 sc1
	s_mov_b64 exec, s[100:101]
	s_mov_b64 s[98:99], exec
	s_andn2_b64 exec, exec, s[12:13]
	s_cbranch_execz .Lp4_lastA
	v_lshrrev_b64 v[54:55], 6, v[2:3]
	global_load_dwordx4 v[50:53], v[6:7], off
	v_lshlrev_b32_e32 v86, 1, v2
	v_lshlrev_b64 v[62:63], 7, v[54:55]
	v_and_b32_e32 v56, 0x78, v1
	v_and_b32_e32 v86, 0x60, v86
	v_lshl_add_u64 v[62:63], s[94:95], 0, v[62:63]
	v_lshlrev_b64 v[64:65], 11, v[54:55]
	v_lshlrev_b32_e32 v66, 2, v56
	v_lshl_add_u64 v[62:63], v[62:63], 0, v[86:87]
	global_load_dwordx4 v[54:57], v66, s[22:23]
	global_load_dwordx4 v[58:61], v66, s[22:23] offset:16
	v_lshl_add_u64 v[66:67], s[8:9], 0, v[64:65]
	global_load_dwordx4 v[62:65], v[62:63], off
	v_and_b32_e32 v88, 0x1f8, v1
	v_lshlrev_b32_e32 v86, 1, v88
	v_lshl_add_u64 v[70:71], v[66:67], 0, v[86:87]
	global_load_dwordx4 v[66:69], v[70:71], off
	v_lshl_add_u64 v[2:3], v[2:3], 0, s[6:7]
	v_cmp_lt_u64_e32 vcc, s[14:15], v[2:3]
	s_or_b64 s[12:13], vcc, s[12:13]
	v_lshl_add_u64 v[6:7], v[6:7], 0, s[10:11]
	v_add_u32_e32 v1, s3, v1
	s_mov_b64 s[100:101], exec
	s_mov_b64 exec, s[98:99]
	s_waitcnt vmcnt(6)
; __device__ __forceinline__ unsigned pk2(float lo, float hi) { return f2bf(lo) | (f2bf(hi) << 16); }
; __device__ __forceinline__ float siluf_(float x) { return x * __builtin_amdgcn_rcpf(1.0f + __expf(-x)); }
; __device__ __forceinline__ void gdn_gate_norm(const Params& P, size_t wi, size_t nw) {
;     ...
;     for (size_t i = wi; i < (size_t)T * 64; i += nw) {
;         const size_t t = i >> 6; const int c0 = (int)(i & 63) * 8, h = c0 >> 7;
;         const f32x4 q0 = *(const f32x4*)(SSQG + t * 32 + h * 8);
;         const float rstd = rsqrtf(((q0.x + q0.y) + (q0.z + q0.w)) * (1.0f / 128.0f) + 1e-6f);
;         const v4u o = *(const v4u*)(Y + t * 1024 + c0), z = Z[i];
;         const f32x4 w0 = *(const f32x4*)(P.gdn_norm_w + (c0 & 127)), w1 = *(const f32x4*)(P.gdn_norm_w + (c0 & 127) + 4);
;         float y[8];
;         y[0] = bflo(o.x) * rstd * w0.x * siluf_(bflo(z.x)); y[1] = bfhi(o.x) * rstd * w0.y * siluf_(bfhi(z.x));
;         y[2] = bflo(o.y) * rstd * w0.z * siluf_(bflo(z.y)); y[3] = bfhi(o.y) * rstd * w0.w * siluf_(bfhi(z.y));
;         y[4] = bflo(o.z) * rstd * w1.x * siluf_(bflo(z.z)); y[5] = bfhi(o.z) * rstd * w1.y * siluf_(bfhi(z.z));
;         y[6] = bflo(o.w) * rstd * w1.z * siluf_(bflo(z.w)); y[7] = bfhi(o.w) * rstd * w1.w * siluf_(bfhi(z.w));
;         v4u r; r.x = pk2(y[0], y[1]); r.y = pk2(y[2], y[3]); r.z = pk2(y[4], y[5]); r.w = pk2(y[6], y[7]);
;         *(v4u*)(Y + t * 1024 + c0) = r;
;     }
	v_lshlrev_b32_e32 v32, 16, v10
	v_mul_f32_e32 v4, 0xbfb8aa3b, v32
	v_exp_f32_e32 v4, v4
	v_lshlrev_b32_e32 v33, 16, v11
	v_lshlrev_b32_e32 v35, 16, v13
	v_lshlrev_b32_e32 v34, 16, v12
	v_and_b32_e32 v13, 0xffff0000, v13
	v_and_b32_e32 v12, 0xffff0000, v12
	v_mov_b32_e32 v36, v14
	v_mov_b32_e32 v37, v16
	v_mov_b32_e32 v16, v15
	v_mov_b32_e32 v14, v18
	v_mov_b32_e32 v15, v20
	v_mov_b32_e32 v20, v19
	v_mov_b32_e32 v18, v23
	v_mov_b32_e32 v19, v24
	v_mov_b32_e32 v23, v25
	v_pk_add_f32 v[18:19], v[18:19], v[22:23]
	v_and_b32_e32 v11, 0xffff0000, v11
	v_add_f32_e32 v18, v18, v19
	v_and_b32_e32 v10, 0xffff0000, v10
	v_mul_f32_e32 v38, 0xbfb8aa3b, v33
	v_mul_f32_e32 v40, 0xbfb8aa3b, v34
	v_mul_f32_e32 v41, 0xbfb8aa3b, v12
	v_mul_f32_e32 v42, 0xbfb8aa3b, v35
	v_mul_f32_e32 v43, 0xbfb8aa3b, v13
	v_add_f32_e32 v4, 1.0, v4
	v_fmamk_f32 v45, v18, 0x3c000000, v8
	v_mul_f32_e32 v9, 0xbfb8aa3b, v10
	v_mul_f32_e32 v39, 0xbfb8aa3b, v11
	v_exp_f32_e32 v38, v38
	v_exp_f32_e32 v40, v40
	v_exp_f32_e32 v41, v41
	v_exp_f32_e32 v42, v42
	v_exp_f32_e32 v43, v43
	v_rcp_f32_e32 v18, v4
	v_mul_f32_e32 v4, 0x4b800000, v45
	v_cmp_gt_f32_e32 vcc, s16, v45
	v_exp_f32_e32 v9, v9
	v_exp_f32_e32 v39, v39
	v_cndmask_b32_e32 v4, v45, v4, vcc
	v_rsq_f32_e32 v4, v4
	v_add_f32_e32 v19, 1.0, v38
	v_add_f32_e32 v40, 1.0, v40
	v_add_f32_e32 v41, 1.0, v41
	v_add_f32_e32 v44, 1.0, v42
	v_add_f32_e32 v43, 1.0, v43
	v_add_f32_e32 v9, 1.0, v9
	v_add_f32_e32 v39, 1.0, v39
	v_rcp_f32_e32 v19, v19
	v_rcp_f32_e32 v40, v40
	v_rcp_f32_e32 v42, v41
	v_rcp_f32_e32 v41, v44
	v_rcp_f32_e32 v43, v43
	v_rcp_f32_e32 v38, v9
	v_rcp_f32_e32 v39, v39
	v_mul_f32_e32 v9, 0x45800000, v4
	v_lshlrev_b32_e32 v23, 16, v27
	v_lshlrev_b32_e32 v22, 16, v26
	v_and_b32_e32 v25, 0xffff0000, v27
	v_and_b32_e32 v24, 0xffff0000, v26
	v_lshlrev_b32_e32 v27, 16, v29
	v_lshlrev_b32_e32 v26, 16, v28
	v_and_b32_e32 v29, 0xffff0000, v29
	v_and_b32_e32 v28, 0xffff0000, v28
	v_cndmask_b32_e32 v4, v4, v9, vcc
	v_pk_mul_f32 v[22:23], v[4:5], v[22:23] op_sel_hi:[0,1]
	v_pk_mul_f32 v[26:27], v[4:5], v[26:27] op_sel_hi:[0,1]
	v_pk_mul_f32 v[28:29], v[4:5], v[28:29] op_sel_hi:[0,1]
	v_pk_mul_f32 v[18:19], v[18:19], v[32:33]
	v_pk_mul_f32 v[32:33], v[40:41], v[34:35]
	v_pk_mul_f32 v[12:13], v[42:43], v[12:13]
	v_pk_mul_f32 v[24:25], v[4:5], v[24:25] op_sel_hi:[0,1]
	v_pk_mul_f32 v[22:23], v[36:37], v[22:23]
	v_pk_mul_f32 v[14:15], v[14:15], v[26:27]
	v_pk_mul_f32 v[20:21], v[20:21], v[28:29]
	v_pk_mul_f32 v[10:11], v[38:39], v[10:11]
	v_pk_mul_f32 v[16:17], v[16:17], v[24:25]
	v_pk_mul_f32 v[18:19], v[18:19], v[22:23]
	v_pk_mul_f32 v[14:15], v[32:33], v[14:15]
	v_pk_mul_f32 v[12:13], v[12:13], v[20:21]
	v_pk_mul_f32 v[10:11], v[10:11], v[16:17]
	v_cvt_pk_bf16_f32 v10, v18, v10
	v_cvt_pk_bf16_f32 v11, v19, v11
	v_cvt_pk_bf16_f32 v12, v14, v12
	v_cvt_pk_bf16_f32 v13, v15, v13
	global_store_dwordx4 v[30:31], v[10:13], off sc0 sc1
	s_mov_b64 exec, s[100:101]
	s_branch .Lp4_loop
.Lp4_lastA:
	s_mov_b64 exec, s[98:99]
	s_waitcnt vmcnt(0)
	v_lshlrev_b32_e32 v32, 16, v10
	v_mul_f32_e32 v4, 0xbfb8aa3b, v32
	v_exp_f32_e32 v4, v4
	v_lshlrev_b32_e32 v33, 16, v11
	v_lshlrev_b32_e32 v35, 16, v13
	v_lshlrev_b32_e32 v34, 16, v12
	v_and_b32_e32 v13, 0xffff0000, v13
	v_and_b32_e32 v12, 0xffff0000, v12
	v_mov_b32_e32 v36, v14
	v_mov_b32_e32 v37, v16
	v_mov_b32_e32 v16, v15
	v_mov_b32_e32 v14, v18
	v_mov_b32_e32 v15, v20
	v_mov_b32_e32 v20, v19
	v_mov_b32_e32 v18, v23
	v_mov_b32_e32 v19, v24
	v_mov_b32_e32 v23, v25
	v_pk_add_f32 v[18:19], v[18:19], v[22:23]
	v_and_b32_e32 v11, 0xffff0000, v11
	v_add_f32_e32 v18, v18, v19
	v_and_b32_e32 v10, 0xffff0000, v10
	v_mul_f32_e32 v38, 0xbfb8aa3b, v33
	v_mul_f32_e32 v40, 0xbfb8aa3b, v34
	v_mul_f32_e32 v41, 0xbfb8aa3b, v12
	v_mul_f32_e32 v42, 0xbfb8aa3b, v35
	v_mul_f32_e32 v43, 0xbfb8aa3b, v13
	v_add_f32_e32 v4, 1.0, v4
	v_fmamk_f32 v45, v18, 0x3c000000, v8
	v_mul_f32_e32 v9, 0xbfb8aa3b, v10
	v_mul_f32_e32 v39, 0xbfb8aa3b, v11
	v_exp_f32_e32 v38, v38
	v_exp_f32_e32 v40, v40
	v_exp_f32_e32 v41, v41
	v_exp_f32_e32 v42, v42
	v_exp_f32_e32 v43, v43
	v_rcp_f32_e32 v18, v4
	v_mul_f32_e32 v4, 0x4b800000, v45
	v_cmp_gt_f32_e32 vcc, s16, v45
	v_exp_f32_e32 v9, v9
	v_exp_f32_e32 v39, v39
	v_cndmask_b32_e32 v4, v45, v4, vcc
	v_rsq_f32_e32 v4, v4
	v_add_f32_e32 v19, 1.0, v38
	v_add_f32_e32 v40, 1.0, v40
	v_add_f32_e32 v41, 1.0, v41
	v_add_f32_e32 v44, 1.0, v42
	v_add_f32_e32 v43, 1.0, v43
	v_add_f32_e32 v9, 1.0, v9
	v_add_f32_e32 v39, 1.0, v39
	v_rcp_f32_e32 v19, v19
	v_rcp_f32_e32 v40, v40
	v_rcp_f32_e32 v42, v41
	v_rcp_f32_e32 v41, v44
	v_rcp_f32_e32 v43, v43
	v_rcp_f32_e32 v38, v9
	v_rcp_f32_e32 v39, v39
	v_mul_f32_e32 v9, 0x45800000, v4
	v_lshlrev_b32_e32 v23, 16, v27
	v_lshlrev_b32_e32 v22, 16, v26
	v_and_b32_e32 v25, 0xffff0000, v27
	v_and_b32_e32 v24, 0xffff0000, v26
	v_lshlrev_b32_e32 v27, 16, v29
	v_lshlrev_b32_e32 v26, 16, v28
	v_and_b32_e32 v29, 0xffff0000, v29
	v_and_b32_e32 v28, 0xffff0000, v28
	v_cndmask_b32_e32 v4, v4, v9, vcc
	v_pk_mul_f32 v[22:23], v[4:5], v[22:23] op_sel_hi:[0,1]
	v_pk_mul_f32 v[26:27], v[4:5], v[26:27] op_sel_hi:[0,1]
	v_pk_mul_f32 v[28:29], v[4:5], v[28:29] op_sel_hi:[0,1]
	v_pk_mul_f32 v[18:19], v[18:19], v[32:33]
	v_pk_mul_f32 v[32:33], v[40:41], v[34:35]
	v_pk_mul_f32 v[12:13], v[42:43], v[12:13]
	v_pk_mul_f32 v[24:25], v[4:5], v[24:25] op_sel_hi:[0,1]
	v_pk_mul_f32 v[22:23], v[36:37], v[22:23]
	v_pk_mul_f32 v[14:15], v[14:15], v[26:27]
	v_pk_mul_f32 v[20:21], v[20:21], v[28:29]
	v_pk_mul_f32 v[10:11], v[38:39], v[10:11]
	v_pk_mul_f32 v[16:17], v[16:17], v[24:25]
	v_pk_mul_f32 v[18:19], v[18:19], v[22:23]
	v_pk_mul_f32 v[14:15], v[32:33], v[14:15]
	v_pk_mul_f32 v[12:13], v[12:13], v[20:21]
	v_pk_mul_f32 v[10:11], v[10:11], v[16:17]
	v_cvt_pk_bf16_f32 v10, v18, v10
	v_cvt_pk_bf16_f32 v11, v19, v11
	v_cvt_pk_bf16_f32 v12, v14, v12
	v_cvt_pk_bf16_f32 v13, v15, v13
	global_store_dwordx4 v[30:31], v[10:13], off sc0 sc1
	s_branch .Lp4_done
; __device__ __forceinline__ unsigned pk2(float lo, float hi) { return f2bf(lo) | (f2bf(hi) << 16); }
; __device__ __forceinline__ float siluf_(float x) { return x * __builtin_amdgcn_rcpf(1.0f + __expf(-x)); }
; __device__ __forceinline__ void gdn_gate_norm(const Params& P, size_t wi, size_t nw) {
;     ...
;     for (size_t i = wi; i < (size_t)T * 64; i += nw) {
;         const size_t t = i >> 6; const int c0 = (int)(i & 63) * 8, h = c0 >> 7;
;         const f32x4 q0 = *(const f32x4*)(SSQG + t * 32 + h * 8);
;         const float rstd = rsqrtf(((q0.x + q0.y) + (q0.z + q0.w)) * (1.0f / 128.0f) + 1e-6f);
;         const v4u o = *(const v4u*)(Y + t * 1024 + c0), z = Z[i];
;         const f32x4 w0 = *(const f32x4*)(P.gdn_norm_w + (c0 & 127)), w1 = *(const f32x4*)(P.gdn_norm_w + (c0 & 127) + 4);
;         float y[8];
;         y[0] = bflo(o.x) * rstd * w0.x * siluf_(bflo(z.x)); y[1] = bfhi(o.x) * rstd * w0.y * siluf_(bfhi(z.x));
;         y[2] = bflo(o.y) * rstd * w0.z * siluf_(bflo(z.y)); y[3] = bfhi(o.y) * rstd * w0.w * siluf_(bfhi(z.y));
;         y[4] = bflo(o.z) * rstd * w1.x * siluf_(bflo(z.z)); y[5] = bfhi(o.z) * rstd * w1.y * siluf_(bfhi(z.z));
;         y[6] = bflo(o.w) * rstd * w1.z * siluf_(bflo(z.w)); y[7] = bfhi(o.w) * rstd * w1.w * siluf_(bfhi(z.w));
;         v4u r; r.x = pk2(y[0], y[1]); r.y = pk2(y[2], y[3]); r.z = pk2(y[4], y[5]); r.w = pk2(y[6], y[7]);
;         *(v4u*)(Y + t * 1024 + c0) = r;
;     }
.Lp4_lastB:
	s_mov_b64 exec, s[98:99]
	s_waitcnt vmcnt(0)
	v_lshlrev_b32_e32 v72, 16, v50
	v_mul_f32_e32 v86, 0xbfb8aa3b, v72
	v_exp_f32_e32 v86, v86
	v_lshlrev_b32_e32 v73, 16, v51
	v_lshlrev_b32_e32 v75, 16, v53
	v_lshlrev_b32_e32 v74, 16, v52
	v_and_b32_e32 v53, 0xffff0000, v53
	v_and_b32_e32 v52, 0xffff0000, v52
	v_mov_b32_e32 v76, v54
	v_mov_b32_e32 v77, v56
	v_mov_b32_e32 v56, v55
	v_mov_b32_e32 v54, v58
	v_mov_b32_e32 v55, v60
	v_mov_b32_e32 v60, v59
	v_mov_b32_e32 v58, v63
	v_mov_b32_e32 v59, v64
	v_mov_b32_e32 v63, v65
	v_pk_add_f32 v[58:59], v[58:59], v[62:63]
	v_and_b32_e32 v51, 0xffff0000, v51
	v_add_f32_e32 v58, v58, v59
	v_and_b32_e32 v50, 0xffff0000, v50
	v_mul_f32_e32 v78, 0xbfb8aa3b, v73
	v_mul_f32_e32 v80, 0xbfb8aa3b, v74
	v_mul_f32_e32 v81, 0xbfb8aa3b, v52
	v_mul_f32_e32 v82, 0xbfb8aa3b, v75
	v_mul_f32_e32 v83, 0xbfb8aa3b, v53
	v_add_f32_e32 v86, 1.0, v86
	v_fmamk_f32 v85, v58, 0x3c000000, v8
	v_mul_f32_e32 v88, 0xbfb8aa3b, v50
	v_mul_f32_e32 v79, 0xbfb8aa3b, v51
	v_exp_f32_e32 v78, v78
	v_exp_f32_e32 v80, v80
	v_exp_f32_e32 v81, v81
	v_exp_f32_e32 v82, v82
	v_exp_f32_e32 v83, v83
	v_rcp_f32_e32 v58, v86
	v_mul_f32_e32 v86, 0x4b800000, v85
	v_cmp_gt_f32_e32 vcc, s16, v85
	v_exp_f32_e32 v88, v88
	v_exp_f32_e32 v79, v79
	v_cndmask_b32_e32 v86, v85, v86, vcc
	v_rsq_f32_e32 v86, v86
	v_add_f32_e32 v59, 1.0, v78
	v_add_f32_e32 v80, 1.0, v80
	v_add_f32_e32 v81, 1.0, v81
	v_add_f32_e32 v84, 1.0, v82
	v_add_f32_e32 v83, 1.0, v83
	v_add_f32_e32 v88, 1.0, v88
	v_add_f32_e32 v79, 1.0, v79
	v_rcp_f32_e32 v59, v59
	v_rcp_f32_e32 v80, v80
	v_rcp_f32_e32 v82, v81
	v_rcp_f32_e32 v81, v84
	v_rcp_f32_e32 v83, v83
	v_rcp_f32_e32 v78, v88
	v_rcp_f32_e32 v79, v79
	v_mul_f32_e32 v88, 0x45800000, v86
	v_lshlrev_b32_e32 v63, 16, v67
	v_lshlrev_b32_e32 v62, 16, v66
	v_and_b32_e32 v65, 0xffff0000, v67
	v_and_b32_e32 v64, 0xffff0000, v66
	v_lshlrev_b32_e32 v67, 16, v69
	v_lshlrev_b32_e32 v66, 16, v68
	v_and_b32_e32 v69, 0xffff0000, v69
	v_and_b32_e32 v68, 0xffff0000, v68
	v_cndmask_b32_e32 v86, v86, v88, vcc
	v_pk_mul_f32 v[62:63], v[86:87], v[62:63] op_sel_hi:[0,1]
	v_pk_mul_f32 v[66:67], v[86:87], v[66:67] op_sel_hi:[0,1]
	v_pk_mul_f32 v[68:69], v[86:87], v[68:69] op_sel_hi:[0,1]
	v_pk_mul_f32 v[58:59], v[58:59], v[72:73]
	v_pk_mul_f32 v[72:73], v[80:81], v[74:75]
	v_pk_mul_f32 v[52:53], v[82:83], v[52:53]
	v_pk_mul_f32 v[64:65], v[86:87], v[64:65] op_sel_hi:[0,1]
	v_pk_mul_f32 v[62:63], v[76:77], v[62:63]
	v_pk_mul_f32 v[54:55], v[54:55], v[66:67]
	v_pk_mul_f32 v[60:61], v[60:61], v[68:69]
	v_pk_mul_f32 v[50:51], v[78:79], v[50:51]
	v_pk_mul_f32 v[56:57], v[56:57], v[64:65]
	v_pk_mul_f32 v[58:59], v[58:59], v[62:63]
	v_pk_mul_f32 v[54:55], v[72:73], v[54:55]
	v_pk_mul_f32 v[52:53], v[52:53], v[60:61]
	v_pk_mul_f32 v[50:51], v[50:51], v[56:57]
	v_cvt_pk_bf16_f32 v50, v58, v50
	v_cvt_pk_bf16_f32 v51, v59, v51
	v_cvt_pk_bf16_f32 v52, v54, v52
	v_cvt_pk_bf16_f32 v53, v55, v53
	global_store_dwordx4 v[70:71], v[50:53], off sc0 sc1
